# serialized load-wait loops unrolled: moe_sort counting loop (32 round trips), router weight LDS fill (8), NA bias table fill (8); plus earlier changes
# baseline (speedup 1.0000x reference)
.LBB0_871:
	s_mul_i32 s2, s4, 0x1d1
	v_add_lshl_u32 v96, v222, s2, 2
	v_lshl_add_u64 v[0:1], s[18:19], 0, v[96:97]
	global_load_dword v238, v[0:1], off
	global_load_dword v239, v[0:1], off offset:256
	global_load_dword v240, v[0:1], off offset:512
	global_load_dword v241, v[0:1], off offset:768
	global_load_dword v242, v[0:1], off offset:1024
	global_load_dword v243, v[0:1], off offset:1280
	global_load_dword v244, v[0:1], off offset:1536
	v_cmp_gt_u32_e32 vcc, 17, v222
	s_and_saveexec_b64 s[2:3], vcc
	global_load_dword v245, v[0:1], off offset:1792
	s_or_b64 exec, exec, s[2:3]
	s_waitcnt vmcnt(0)
	v_mul_f32_e32 v238, 0x3fb8aa3b, v238
	v_mul_f32_e32 v239, 0x3fb8aa3b, v239
	v_mul_f32_e32 v240, 0x3fb8aa3b, v240
	v_mul_f32_e32 v241, 0x3fb8aa3b, v241
	v_mul_f32_e32 v242, 0x3fb8aa3b, v242
	v_mul_f32_e32 v243, 0x3fb8aa3b, v243
	v_mul_f32_e32 v244, 0x3fb8aa3b, v244
	v_mul_f32_e32 v245, 0x3fb8aa3b, v245
	ds_write_b32 v227, v238
	ds_write_b32 v227, v239 offset:256
	ds_write_b32 v227, v240 offset:512
	ds_write_b32 v227, v241 offset:768
	ds_write_b32 v227, v242 offset:1024
	ds_write_b32 v227, v243 offset:1280
	ds_write_b32 v227, v244 offset:1536
	s_and_saveexec_b64 s[2:3], vcc
	ds_write_b32 v227, v245 offset:1792
	s_or_b64 exec, exec, s[2:3]
	s_mov_b32 s31, 24

.LBB0_1538:
	s_andn2_b64 vcc, exec, s[4:5]
	s_cbranch_vccnz .LBB0_1549
	v_cmp_gt_i32_e32 vcc, s57, v101
	s_barrier
	s_and_saveexec_b64 s[4:5], vcc
	v_readlane_b32 s16, v254, 23
	v_readlane_b32 s24, v254, 31
	v_readlane_b32 s25, v254, 32
	v_readlane_b32 s17, v254, 24
	v_readlane_b32 s18, v254, 25
	v_readlane_b32 s19, v254, 26
	v_readlane_b32 s20, v254, 27
	v_readlane_b32 s21, v254, 28
	v_readlane_b32 s22, v254, 29
	v_readlane_b32 s23, v254, 30
	v_readlane_b32 s26, v254, 33
	v_readlane_b32 s27, v254, 34
	v_readlane_b32 s28, v254, 35
	v_readlane_b32 s29, v254, 36
	v_readlane_b32 s30, v254, 37
	v_readlane_b32 s31, v254, 38
	s_cbranch_execz .LBB0_1542
	v_lshlrev_b32_e32 v0, 2, v101
	s_mov_b64 s[8:9], 0
	s_waitcnt vmcnt(0)
	v_ashrrev_i32_e32 v6, 1, v101
	v_ashrrev_i32_e32 v7, 31, v6
	v_lshlrev_b64 v[2:3], 5, v[6:7]
	v_lshlrev_b32_e32 v1, 2, v0
	v_lshl_add_u64 v[2:3], s[24:25], 0, v[2:3]
	v_and_b32_e32 v96, 16, v1
	v_lshl_add_u64 v[2:3], v[2:3], 0, v[96:97]
	global_load_dwordx4 v[128:131], v[2:3], off
	v_lshrrev_b32_e32 v1, 7, v101
	v_and_b32_e32 v6, 3, v6
	s_mov_b32 s10, 0x1ffffc
	v_and_or_b32 v1, v1, s10, v6
	v_and_b32_e32 v6, 0x1f8, v101
	v_lshl_add_u32 v1, v1, 11, 0
	v_lshlrev_b32_e32 v6, 2, v6
	v_add3_u32 v160, v1, v6, v96
	v_add_u32_e32 v0, 0x800, v0
	v_add_u32_e32 v101, 0x200, v101
	v_ashrrev_i32_e32 v6, 1, v101
	v_ashrrev_i32_e32 v7, 31, v6
	v_lshlrev_b64 v[2:3], 5, v[6:7]
	v_lshlrev_b32_e32 v1, 2, v0
	v_lshl_add_u64 v[2:3], s[24:25], 0, v[2:3]
	v_and_b32_e32 v96, 16, v1
	v_lshl_add_u64 v[2:3], v[2:3], 0, v[96:97]
	global_load_dwordx4 v[132:135], v[2:3], off
	v_lshrrev_b32_e32 v1, 7, v101
	v_and_b32_e32 v6, 3, v6
	s_mov_b32 s10, 0x1ffffc
	v_and_or_b32 v1, v1, s10, v6
	v_and_b32_e32 v6, 0x1f8, v101
	v_lshl_add_u32 v1, v1, 11, 0
	v_lshlrev_b32_e32 v6, 2, v6
	v_add3_u32 v161, v1, v6, v96
	v_add_u32_e32 v0, 0x800, v0
	v_add_u32_e32 v101, 0x200, v101
	v_ashrrev_i32_e32 v6, 1, v101
	v_ashrrev_i32_e32 v7, 31, v6
	v_lshlrev_b64 v[2:3], 5, v[6:7]
	v_lshlrev_b32_e32 v1, 2, v0
	v_lshl_add_u64 v[2:3], s[24:25], 0, v[2:3]
	v_and_b32_e32 v96, 16, v1
	v_lshl_add_u64 v[2:3], v[2:3], 0, v[96:97]
	global_load_dwordx4 v[136:139], v[2:3], off
	v_lshrrev_b32_e32 v1, 7, v101
	v_and_b32_e32 v6, 3, v6
	s_mov_b32 s10, 0x1ffffc
	v_and_or_b32 v1, v1, s10, v6
	v_and_b32_e32 v6, 0x1f8, v101
	v_lshl_add_u32 v1, v1, 11, 0
	v_lshlrev_b32_e32 v6, 2, v6
	v_add3_u32 v162, v1, v6, v96
	v_add_u32_e32 v0, 0x800, v0
	v_add_u32_e32 v101, 0x200, v101
	v_ashrrev_i32_e32 v6, 1, v101
	v_ashrrev_i32_e32 v7, 31, v6
	v_lshlrev_b64 v[2:3], 5, v[6:7]
	v_lshlrev_b32_e32 v1, 2, v0
	v_lshl_add_u64 v[2:3], s[24:25], 0, v[2:3]
	v_and_b32_e32 v96, 16, v1
	v_lshl_add_u64 v[2:3], v[2:3], 0, v[96:97]
	global_load_dwordx4 v[140:143], v[2:3], off
	v_lshrrev_b32_e32 v1, 7, v101
	v_and_b32_e32 v6, 3, v6
	s_mov_b32 s10, 0x1ffffc
	v_and_or_b32 v1, v1, s10, v6
	v_and_b32_e32 v6, 0x1f8, v101
	v_lshl_add_u32 v1, v1, 11, 0
	v_lshlrev_b32_e32 v6, 2, v6
	v_add3_u32 v163, v1, v6, v96
	v_add_u32_e32 v0, 0x800, v0
	v_add_u32_e32 v101, 0x200, v101
	v_ashrrev_i32_e32 v6, 1, v101
	v_ashrrev_i32_e32 v7, 31, v6
	v_lshlrev_b64 v[2:3], 5, v[6:7]
	v_lshlrev_b32_e32 v1, 2, v0
	v_lshl_add_u64 v[2:3], s[24:25], 0, v[2:3]
	v_and_b32_e32 v96, 16, v1
	v_lshl_add_u64 v[2:3], v[2:3], 0, v[96:97]
	global_load_dwordx4 v[144:147], v[2:3], off
	v_lshrrev_b32_e32 v1, 7, v101
	v_and_b32_e32 v6, 3, v6
	s_mov_b32 s10, 0x1ffffc
	v_and_or_b32 v1, v1, s10, v6
	v_and_b32_e32 v6, 0x1f8, v101
	v_lshl_add_u32 v1, v1, 11, 0
	v_lshlrev_b32_e32 v6, 2, v6
	v_add3_u32 v164, v1, v6, v96
	v_add_u32_e32 v0, 0x800, v0
	v_add_u32_e32 v101, 0x200, v101
	v_ashrrev_i32_e32 v6, 1, v101
	v_ashrrev_i32_e32 v7, 31, v6
	v_lshlrev_b64 v[2:3], 5, v[6:7]
	v_lshlrev_b32_e32 v1, 2, v0
	v_lshl_add_u64 v[2:3], s[24:25], 0, v[2:3]
	v_and_b32_e32 v96, 16, v1
	v_lshl_add_u64 v[2:3], v[2:3], 0, v[96:97]
	global_load_dwordx4 v[148:151], v[2:3], off
	v_lshrrev_b32_e32 v1, 7, v101
	v_and_b32_e32 v6, 3, v6
	s_mov_b32 s10, 0x1ffffc
	v_and_or_b32 v1, v1, s10, v6
	v_and_b32_e32 v6, 0x1f8, v101
	v_lshl_add_u32 v1, v1, 11, 0
	v_lshlrev_b32_e32 v6, 2, v6
	v_add3_u32 v165, v1, v6, v96
	v_add_u32_e32 v0, 0x800, v0
	v_add_u32_e32 v101, 0x200, v101
	v_ashrrev_i32_e32 v6, 1, v101
	v_ashrrev_i32_e32 v7, 31, v6
	v_lshlrev_b64 v[2:3], 5, v[6:7]
	v_lshlrev_b32_e32 v1, 2, v0
	v_lshl_add_u64 v[2:3], s[24:25], 0, v[2:3]
	v_and_b32_e32 v96, 16, v1
	v_lshl_add_u64 v[2:3], v[2:3], 0, v[96:97]
	global_load_dwordx4 v[152:155], v[2:3], off
	v_lshrrev_b32_e32 v1, 7, v101
	v_and_b32_e32 v6, 3, v6
	s_mov_b32 s10, 0x1ffffc
	v_and_or_b32 v1, v1, s10, v6
	v_and_b32_e32 v6, 0x1f8, v101
	v_lshl_add_u32 v1, v1, 11, 0
	v_lshlrev_b32_e32 v6, 2, v6
	v_add3_u32 v166, v1, v6, v96
	v_add_u32_e32 v0, 0x800, v0
	v_add_u32_e32 v101, 0x200, v101
	v_ashrrev_i32_e32 v6, 1, v101
	v_ashrrev_i32_e32 v7, 31, v6
	v_lshlrev_b64 v[2:3], 5, v[6:7]
	v_lshlrev_b32_e32 v1, 2, v0
	v_lshl_add_u64 v[2:3], s[24:25], 0, v[2:3]
	v_and_b32_e32 v96, 16, v1
	v_lshl_add_u64 v[2:3], v[2:3], 0, v[96:97]
	global_load_dwordx4 v[156:159], v[2:3], off
	v_lshrrev_b32_e32 v1, 7, v101
	v_and_b32_e32 v6, 3, v6
	s_mov_b32 s10, 0x1ffffc
	v_and_or_b32 v1, v1, s10, v6
	v_and_b32_e32 v6, 0x1f8, v101
	v_lshl_add_u32 v1, v1, 11, 0
	v_lshlrev_b32_e32 v6, 2, v6
	v_add3_u32 v167, v1, v6, v96
	v_add_u32_e32 v0, 0x800, v0
	v_add_u32_e32 v101, 0x200, v101
	s_waitcnt vmcnt(7)
	ds_write_b128 v160, v[128:131]
	s_waitcnt vmcnt(6)
	ds_write_b128 v161, v[132:135]
	s_waitcnt vmcnt(5)
	ds_write_b128 v162, v[136:139]
	s_waitcnt vmcnt(4)
	ds_write_b128 v163, v[140:143]
	s_waitcnt vmcnt(3)
	ds_write_b128 v164, v[144:147]
	s_waitcnt vmcnt(2)
	ds_write_b128 v165, v[148:151]
	s_waitcnt vmcnt(1)
	ds_write_b128 v166, v[152:155]
	s_waitcnt vmcnt(0)
	ds_write_b128 v167, v[156:159]
	s_mov_b64 s[8:9], exec

.LBB0_1603:
	v_readlane_b32 s6, v254, 7
	v_readlane_b32 s7, v254, 8
	s_cmp_le_i32 s6, s22
	s_cselect_b64 s[4:5], -1, 0
	s_cmp_lt_i32 s22, s7
	s_cselect_b64 s[6:7], -1, 0
	s_waitcnt vmcnt(0)
	v_mbcnt_lo_u32_b32 v17, -1, 0
	v_mbcnt_hi_u32_b32 v17, -1, v17
	s_and_b64 s[8:9], s[4:5], s[6:7]
	v_or_b32_e32 v130, s66, v17
	s_mov_b32 s34, s71
	v_readfirstlane_b32 s16, v130
	s_andn2_b64 vcc, exec, s[8:9]
	s_mov_b64 s[4:5], -1
	s_cbranch_vccnz .LBB0_1709
	v_readlane_b32 s6, v255, 35
	v_readlane_b32 s7, v255, 36
	s_mov_b64 s[4:5], 0
	s_and_b64 vcc, exec, s[6:7]
	s_cbranch_vccz .LBB0_1709
	v_lshl_add_u32 v2, v130, 2, 0
	v_cmp_gt_i32_e32 vcc, 16, v130
	s_barrier
	s_and_saveexec_b64 s[4:5], vcc
	ds_write_b32 v2, v97
	s_or_b64 exec, exec, s[4:5]
	s_add_u32 s10, s44, 0x33d18000
	s_addc_u32 s11, s45, 0
	v_cmp_gt_i32_e32 vcc, s62, v130
	s_lshl_b32 s17, s34, 6
	v_ashrrev_i32_e32 v131, 31, v130
	v_mov_b32_e32 v3, 0
	v_mov_b32_e32 v5, 0
	v_mov_b32_e32 v7, 0
	v_mov_b32_e32 v9, 0
	v_mov_b32_e32 v11, 0
	v_mov_b32_e32 v13, 0
	v_mov_b32_e32 v15, 0
	v_mov_b32_e32 v18, 0
	v_mov_b32_e32 v4, 0
	v_mov_b32_e32 v6, 0
	v_mov_b32_e32 v8, 0
	v_mov_b32_e32 v10, 0
	v_mov_b32_e32 v12, 0
	v_mov_b32_e32 v14, 0
	v_mov_b32_e32 v16, 0
	v_mov_b32_e32 v19, 0
	s_waitcnt lgkmcnt(0)
	s_barrier
	s_and_saveexec_b64 s[12:13], vcc
	s_cbranch_execz .LBB0_1611
	v_lshl_add_u64 v[0:1], v[130:131], 2, s[10:11]
	v_mov_b32_e32 v18, 0
	s_mov_b64 s[14:15], 0
	s_waitcnt vmcnt(2)
	v_mov_b32_e32 v20, v130
	v_mov_b32_e32 v15, 0
	v_mov_b32_e32 v13, 0
	v_mov_b32_e32 v11, 0
	v_mov_b32_e32 v9, 0
	v_mov_b32_e32 v7, 0
	v_mov_b32_e32 v5, 0
	v_mov_b32_e32 v3, 0
	v_mov_b32_e32 v19, 0
	v_mov_b32_e32 v16, 0
	v_mov_b32_e32 v14, 0
	v_mov_b32_e32 v12, 0
	v_mov_b32_e32 v10, 0
	v_mov_b32_e32 v8, 0
	v_mov_b32_e32 v6, 0
	v_mov_b32_e32 v4, 0
	s_mov_b64 s[4:5], 0x800
	global_load_dword v32, v[0:1], off
	v_lshl_add_u64 v[0:1], v[0:1], 0, s[4:5]
	global_load_dword v33, v[0:1], off
	v_lshl_add_u64 v[0:1], v[0:1], 0, s[4:5]
	global_load_dword v34, v[0:1], off
	v_lshl_add_u64 v[0:1], v[0:1], 0, s[4:5]
	global_load_dword v35, v[0:1], off
	v_lshl_add_u64 v[0:1], v[0:1], 0, s[4:5]
	global_load_dword v36, v[0:1], off
	v_lshl_add_u64 v[0:1], v[0:1], 0, s[4:5]
	global_load_dword v37, v[0:1], off
	v_lshl_add_u64 v[0:1], v[0:1], 0, s[4:5]
	global_load_dword v38, v[0:1], off
	v_lshl_add_u64 v[0:1], v[0:1], 0, s[4:5]
	global_load_dword v39, v[0:1], off
	v_lshl_add_u64 v[0:1], v[0:1], 0, s[4:5]
	global_load_dword v40, v[0:1], off
	v_lshl_add_u64 v[0:1], v[0:1], 0, s[4:5]
	global_load_dword v41, v[0:1], off
	v_lshl_add_u64 v[0:1], v[0:1], 0, s[4:5]
	global_load_dword v42, v[0:1], off
	v_lshl_add_u64 v[0:1], v[0:1], 0, s[4:5]
	global_load_dword v43, v[0:1], off
	v_lshl_add_u64 v[0:1], v[0:1], 0, s[4:5]
	global_load_dword v44, v[0:1], off
	v_lshl_add_u64 v[0:1], v[0:1], 0, s[4:5]
	global_load_dword v45, v[0:1], off
	v_lshl_add_u64 v[0:1], v[0:1], 0, s[4:5]
	global_load_dword v46, v[0:1], off
	v_lshl_add_u64 v[0:1], v[0:1], 0, s[4:5]
	global_load_dword v47, v[0:1], off
	v_lshl_add_u64 v[0:1], v[0:1], 0, s[4:5]
	global_load_dword v48, v[0:1], off
	v_lshl_add_u64 v[0:1], v[0:1], 0, s[4:5]
	global_load_dword v49, v[0:1], off
	v_lshl_add_u64 v[0:1], v[0:1], 0, s[4:5]
	global_load_dword v50, v[0:1], off
	v_lshl_add_u64 v[0:1], v[0:1], 0, s[4:5]
	global_load_dword v51, v[0:1], off
	v_lshl_add_u64 v[0:1], v[0:1], 0, s[4:5]
	global_load_dword v52, v[0:1], off
	v_lshl_add_u64 v[0:1], v[0:1], 0, s[4:5]
	global_load_dword v53, v[0:1], off
	v_lshl_add_u64 v[0:1], v[0:1], 0, s[4:5]
	global_load_dword v54, v[0:1], off
	v_lshl_add_u64 v[0:1], v[0:1], 0, s[4:5]
	global_load_dword v55, v[0:1], off
	v_lshl_add_u64 v[0:1], v[0:1], 0, s[4:5]
	global_load_dword v56, v[0:1], off
	v_lshl_add_u64 v[0:1], v[0:1], 0, s[4:5]
	global_load_dword v57, v[0:1], off
	v_lshl_add_u64 v[0:1], v[0:1], 0, s[4:5]
	global_load_dword v58, v[0:1], off
	v_lshl_add_u64 v[0:1], v[0:1], 0, s[4:5]
	global_load_dword v59, v[0:1], off
	v_lshl_add_u64 v[0:1], v[0:1], 0, s[4:5]
	global_load_dword v60, v[0:1], off
	v_lshl_add_u64 v[0:1], v[0:1], 0, s[4:5]
	global_load_dword v61, v[0:1], off
	v_lshl_add_u64 v[0:1], v[0:1], 0, s[4:5]
	global_load_dword v62, v[0:1], off
	v_lshl_add_u64 v[0:1], v[0:1], 0, s[4:5]
	global_load_dword v63, v[0:1], off
	v_cmp_gt_i32_e32 vcc, s17, v20
	s_waitcnt vmcnt(31)
	v_cmp_eq_u32_e64 s[4:5], 0, v32
	s_nop 1
	v_addc_co_u32_e64 v18, s[6:7], 0, v18, s[4:5]
	s_and_b64 s[4:5], s[4:5], vcc
	v_addc_co_u32_e64 v19, s[4:5], 0, v19, s[4:5]
	v_cmp_eq_u32_e64 s[4:5], 1, v32
	s_nop 1
	v_addc_co_u32_e64 v15, s[6:7], 0, v15, s[4:5]
	s_and_b64 s[4:5], s[4:5], vcc
	v_addc_co_u32_e64 v16, s[4:5], 0, v16, s[4:5]
	v_cmp_eq_u32_e64 s[4:5], 2, v32
	s_nop 1
	v_addc_co_u32_e64 v13, s[6:7], 0, v13, s[4:5]
	s_and_b64 s[4:5], s[4:5], vcc
	v_addc_co_u32_e64 v14, s[4:5], 0, v14, s[4:5]
	v_cmp_eq_u32_e64 s[4:5], 3, v32
	s_nop 1
	v_addc_co_u32_e64 v11, s[6:7], 0, v11, s[4:5]
	s_and_b64 s[4:5], s[4:5], vcc
	v_addc_co_u32_e64 v12, s[4:5], 0, v12, s[4:5]
	v_cmp_eq_u32_e64 s[4:5], 4, v32
	s_nop 1
	v_addc_co_u32_e64 v9, s[6:7], 0, v9, s[4:5]
	s_and_b64 s[4:5], s[4:5], vcc
	v_addc_co_u32_e64 v10, s[4:5], 0, v10, s[4:5]
	v_cmp_eq_u32_e64 s[4:5], 5, v32
	s_nop 1
	v_addc_co_u32_e64 v7, s[6:7], 0, v7, s[4:5]
	s_and_b64 s[4:5], s[4:5], vcc
	v_addc_co_u32_e64 v8, s[4:5], 0, v8, s[4:5]
	v_cmp_eq_u32_e64 s[4:5], 6, v32
	s_nop 1
	v_addc_co_u32_e64 v5, s[6:7], 0, v5, s[4:5]
	s_and_b64 s[4:5], s[4:5], vcc
	v_addc_co_u32_e64 v6, s[4:5], 0, v6, s[4:5]
	v_cmp_eq_u32_e64 s[4:5], 7, v32
	s_and_b64 vcc, s[4:5], vcc
	v_addc_co_u32_e32 v4, vcc, 0, v4, vcc
	v_addc_co_u32_e64 v3, s[6:7], 0, v3, s[4:5]
	v_add_u32_e32 v20, 0x200, v20
	v_cmp_gt_i32_e32 vcc, s17, v20
	s_waitcnt vmcnt(30)
	v_cmp_eq_u32_e64 s[4:5], 0, v33
	s_nop 1
	v_addc_co_u32_e64 v18, s[6:7], 0, v18, s[4:5]
	s_and_b64 s[4:5], s[4:5], vcc
	v_addc_co_u32_e64 v19, s[4:5], 0, v19, s[4:5]
	v_cmp_eq_u32_e64 s[4:5], 1, v33
	s_nop 1
	v_addc_co_u32_e64 v15, s[6:7], 0, v15, s[4:5]
	s_and_b64 s[4:5], s[4:5], vcc
	v_addc_co_u32_e64 v16, s[4:5], 0, v16, s[4:5]
	v_cmp_eq_u32_e64 s[4:5], 2, v33
	s_nop 1
	v_addc_co_u32_e64 v13, s[6:7], 0, v13, s[4:5]
	s_and_b64 s[4:5], s[4:5], vcc
	v_addc_co_u32_e64 v14, s[4:5], 0, v14, s[4:5]
	v_cmp_eq_u32_e64 s[4:5], 3, v33
	s_nop 1
	v_addc_co_u32_e64 v11, s[6:7], 0, v11, s[4:5]
	s_and_b64 s[4:5], s[4:5], vcc
	v_addc_co_u32_e64 v12, s[4:5], 0, v12, s[4:5]
	v_cmp_eq_u32_e64 s[4:5], 4, v33
	s_nop 1
	v_addc_co_u32_e64 v9, s[6:7], 0, v9, s[4:5]
	s_and_b64 s[4:5], s[4:5], vcc
	v_addc_co_u32_e64 v10, s[4:5], 0, v10, s[4:5]
	v_cmp_eq_u32_e64 s[4:5], 5, v33
	s_nop 1
	v_addc_co_u32_e64 v7, s[6:7], 0, v7, s[4:5]
	s_and_b64 s[4:5], s[4:5], vcc
	v_addc_co_u32_e64 v8, s[4:5], 0, v8, s[4:5]
	v_cmp_eq_u32_e64 s[4:5], 6, v33
	s_nop 1
	v_addc_co_u32_e64 v5, s[6:7], 0, v5, s[4:5]
	s_and_b64 s[4:5], s[4:5], vcc
	v_addc_co_u32_e64 v6, s[4:5], 0, v6, s[4:5]
	v_cmp_eq_u32_e64 s[4:5], 7, v33
	s_and_b64 vcc, s[4:5], vcc
	v_addc_co_u32_e32 v4, vcc, 0, v4, vcc
	v_addc_co_u32_e64 v3, s[6:7], 0, v3, s[4:5]
	v_add_u32_e32 v20, 0x200, v20
	v_cmp_gt_i32_e32 vcc, s17, v20
	s_waitcnt vmcnt(29)
	v_cmp_eq_u32_e64 s[4:5], 0, v34
	s_nop 1
	v_addc_co_u32_e64 v18, s[6:7], 0, v18, s[4:5]
	s_and_b64 s[4:5], s[4:5], vcc
	v_addc_co_u32_e64 v19, s[4:5], 0, v19, s[4:5]
	v_cmp_eq_u32_e64 s[4:5], 1, v34
	s_nop 1
	v_addc_co_u32_e64 v15, s[6:7], 0, v15, s[4:5]
	s_and_b64 s[4:5], s[4:5], vcc
	v_addc_co_u32_e64 v16, s[4:5], 0, v16, s[4:5]
	v_cmp_eq_u32_e64 s[4:5], 2, v34
	s_nop 1
	v_addc_co_u32_e64 v13, s[6:7], 0, v13, s[4:5]
	s_and_b64 s[4:5], s[4:5], vcc
	v_addc_co_u32_e64 v14, s[4:5], 0, v14, s[4:5]
	v_cmp_eq_u32_e64 s[4:5], 3, v34
	s_nop 1
	v_addc_co_u32_e64 v11, s[6:7], 0, v11, s[4:5]
	s_and_b64 s[4:5], s[4:5], vcc
	v_addc_co_u32_e64 v12, s[4:5], 0, v12, s[4:5]
	v_cmp_eq_u32_e64 s[4:5], 4, v34
	s_nop 1
	v_addc_co_u32_e64 v9, s[6:7], 0, v9, s[4:5]
	s_and_b64 s[4:5], s[4:5], vcc
	v_addc_co_u32_e64 v10, s[4:5], 0, v10, s[4:5]
	v_cmp_eq_u32_e64 s[4:5], 5, v34
	s_nop 1
	v_addc_co_u32_e64 v7, s[6:7], 0, v7, s[4:5]
	s_and_b64 s[4:5], s[4:5], vcc
	v_addc_co_u32_e64 v8, s[4:5], 0, v8, s[4:5]
	v_cmp_eq_u32_e64 s[4:5], 6, v34
	s_nop 1
	v_addc_co_u32_e64 v5, s[6:7], 0, v5, s[4:5]
	s_and_b64 s[4:5], s[4:5], vcc
	v_addc_co_u32_e64 v6, s[4:5], 0, v6, s[4:5]
	v_cmp_eq_u32_e64 s[4:5], 7, v34
	s_and_b64 vcc, s[4:5], vcc
	v_addc_co_u32_e32 v4, vcc, 0, v4, vcc
	v_addc_co_u32_e64 v3, s[6:7], 0, v3, s[4:5]
	v_add_u32_e32 v20, 0x200, v20
	v_cmp_gt_i32_e32 vcc, s17, v20
	s_waitcnt vmcnt(28)
	v_cmp_eq_u32_e64 s[4:5], 0, v35
	s_nop 1
	v_addc_co_u32_e64 v18, s[6:7], 0, v18, s[4:5]
	s_and_b64 s[4:5], s[4:5], vcc
	v_addc_co_u32_e64 v19, s[4:5], 0, v19, s[4:5]
	v_cmp_eq_u32_e64 s[4:5], 1, v35
	s_nop 1
	v_addc_co_u32_e64 v15, s[6:7], 0, v15, s[4:5]
	s_and_b64 s[4:5], s[4:5], vcc
	v_addc_co_u32_e64 v16, s[4:5], 0, v16, s[4:5]
	v_cmp_eq_u32_e64 s[4:5], 2, v35
	s_nop 1
	v_addc_co_u32_e64 v13, s[6:7], 0, v13, s[4:5]
	s_and_b64 s[4:5], s[4:5], vcc
	v_addc_co_u32_e64 v14, s[4:5], 0, v14, s[4:5]
	v_cmp_eq_u32_e64 s[4:5], 3, v35
	s_nop 1
	v_addc_co_u32_e64 v11, s[6:7], 0, v11, s[4:5]
	s_and_b64 s[4:5], s[4:5], vcc
	v_addc_co_u32_e64 v12, s[4:5], 0, v12, s[4:5]
	v_cmp_eq_u32_e64 s[4:5], 4, v35
	s_nop 1
	v_addc_co_u32_e64 v9, s[6:7], 0, v9, s[4:5]
	s_and_b64 s[4:5], s[4:5], vcc
	v_addc_co_u32_e64 v10, s[4:5], 0, v10, s[4:5]
	v_cmp_eq_u32_e64 s[4:5], 5, v35
	s_nop 1
	v_addc_co_u32_e64 v7, s[6:7], 0, v7, s[4:5]
	s_and_b64 s[4:5], s[4:5], vcc
	v_addc_co_u32_e64 v8, s[4:5], 0, v8, s[4:5]
	v_cmp_eq_u32_e64 s[4:5], 6, v35
	s_nop 1
	v_addc_co_u32_e64 v5, s[6:7], 0, v5, s[4:5]
	s_and_b64 s[4:5], s[4:5], vcc
	v_addc_co_u32_e64 v6, s[4:5], 0, v6, s[4:5]
	v_cmp_eq_u32_e64 s[4:5], 7, v35
	s_and_b64 vcc, s[4:5], vcc
	v_addc_co_u32_e32 v4, vcc, 0, v4, vcc
	v_addc_co_u32_e64 v3, s[6:7], 0, v3, s[4:5]
	v_add_u32_e32 v20, 0x200, v20
	v_cmp_gt_i32_e32 vcc, s17, v20
	s_waitcnt vmcnt(27)
	v_cmp_eq_u32_e64 s[4:5], 0, v36
	s_nop 1
	v_addc_co_u32_e64 v18, s[6:7], 0, v18, s[4:5]
	s_and_b64 s[4:5], s[4:5], vcc
	v_addc_co_u32_e64 v19, s[4:5], 0, v19, s[4:5]
	v_cmp_eq_u32_e64 s[4:5], 1, v36
	s_nop 1
	v_addc_co_u32_e64 v15, s[6:7], 0, v15, s[4:5]
	s_and_b64 s[4:5], s[4:5], vcc
	v_addc_co_u32_e64 v16, s[4:5], 0, v16, s[4:5]
	v_cmp_eq_u32_e64 s[4:5], 2, v36
	s_nop 1
	v_addc_co_u32_e64 v13, s[6:7], 0, v13, s[4:5]
	s_and_b64 s[4:5], s[4:5], vcc
	v_addc_co_u32_e64 v14, s[4:5], 0, v14, s[4:5]
	v_cmp_eq_u32_e64 s[4:5], 3, v36
	s_nop 1
	v_addc_co_u32_e64 v11, s[6:7], 0, v11, s[4:5]
	s_and_b64 s[4:5], s[4:5], vcc
	v_addc_co_u32_e64 v12, s[4:5], 0, v12, s[4:5]
	v_cmp_eq_u32_e64 s[4:5], 4, v36
	s_nop 1
	v_addc_co_u32_e64 v9, s[6:7], 0, v9, s[4:5]
	s_and_b64 s[4:5], s[4:5], vcc
	v_addc_co_u32_e64 v10, s[4:5], 0, v10, s[4:5]
	v_cmp_eq_u32_e64 s[4:5], 5, v36
	s_nop 1
	v_addc_co_u32_e64 v7, s[6:7], 0, v7, s[4:5]
	s_and_b64 s[4:5], s[4:5], vcc
	v_addc_co_u32_e64 v8, s[4:5], 0, v8, s[4:5]
	v_cmp_eq_u32_e64 s[4:5], 6, v36
	s_nop 1
	v_addc_co_u32_e64 v5, s[6:7], 0, v5, s[4:5]
	s_and_b64 s[4:5], s[4:5], vcc
	v_addc_co_u32_e64 v6, s[4:5], 0, v6, s[4:5]
	v_cmp_eq_u32_e64 s[4:5], 7, v36
	s_and_b64 vcc, s[4:5], vcc
	v_addc_co_u32_e32 v4, vcc, 0, v4, vcc
	v_addc_co_u32_e64 v3, s[6:7], 0, v3, s[4:5]
	v_add_u32_e32 v20, 0x200, v20
	v_cmp_gt_i32_e32 vcc, s17, v20
	s_waitcnt vmcnt(26)
	v_cmp_eq_u32_e64 s[4:5], 0, v37
	s_nop 1
	v_addc_co_u32_e64 v18, s[6:7], 0, v18, s[4:5]
	s_and_b64 s[4:5], s[4:5], vcc
	v_addc_co_u32_e64 v19, s[4:5], 0, v19, s[4:5]
	v_cmp_eq_u32_e64 s[4:5], 1, v37
	s_nop 1
	v_addc_co_u32_e64 v15, s[6:7], 0, v15, s[4:5]
	s_and_b64 s[4:5], s[4:5], vcc
	v_addc_co_u32_e64 v16, s[4:5], 0, v16, s[4:5]
	v_cmp_eq_u32_e64 s[4:5], 2, v37
	s_nop 1
	v_addc_co_u32_e64 v13, s[6:7], 0, v13, s[4:5]
	s_and_b64 s[4:5], s[4:5], vcc
	v_addc_co_u32_e64 v14, s[4:5], 0, v14, s[4:5]
	v_cmp_eq_u32_e64 s[4:5], 3, v37
	s_nop 1
	v_addc_co_u32_e64 v11, s[6:7], 0, v11, s[4:5]
	s_and_b64 s[4:5], s[4:5], vcc
	v_addc_co_u32_e64 v12, s[4:5], 0, v12, s[4:5]
	v_cmp_eq_u32_e64 s[4:5], 4, v37
	s_nop 1
	v_addc_co_u32_e64 v9, s[6:7], 0, v9, s[4:5]
	s_and_b64 s[4:5], s[4:5], vcc
	v_addc_co_u32_e64 v10, s[4:5], 0, v10, s[4:5]
	v_cmp_eq_u32_e64 s[4:5], 5, v37
	s_nop 1
	v_addc_co_u32_e64 v7, s[6:7], 0, v7, s[4:5]
	s_and_b64 s[4:5], s[4:5], vcc
	v_addc_co_u32_e64 v8, s[4:5], 0, v8, s[4:5]
	v_cmp_eq_u32_e64 s[4:5], 6, v37
	s_nop 1
	v_addc_co_u32_e64 v5, s[6:7], 0, v5, s[4:5]
	s_and_b64 s[4:5], s[4:5], vcc
	v_addc_co_u32_e64 v6, s[4:5], 0, v6, s[4:5]
	v_cmp_eq_u32_e64 s[4:5], 7, v37
	s_and_b64 vcc, s[4:5], vcc
	v_addc_co_u32_e32 v4, vcc, 0, v4, vcc
	v_addc_co_u32_e64 v3, s[6:7], 0, v3, s[4:5]
	v_add_u32_e32 v20, 0x200, v20
	v_cmp_gt_i32_e32 vcc, s17, v20
	s_waitcnt vmcnt(25)
	v_cmp_eq_u32_e64 s[4:5], 0, v38
	s_nop 1
	v_addc_co_u32_e64 v18, s[6:7], 0, v18, s[4:5]
	s_and_b64 s[4:5], s[4:5], vcc
	v_addc_co_u32_e64 v19, s[4:5], 0, v19, s[4:5]
	v_cmp_eq_u32_e64 s[4:5], 1, v38
	s_nop 1
	v_addc_co_u32_e64 v15, s[6:7], 0, v15, s[4:5]
	s_and_b64 s[4:5], s[4:5], vcc
	v_addc_co_u32_e64 v16, s[4:5], 0, v16, s[4:5]
	v_cmp_eq_u32_e64 s[4:5], 2, v38
	s_nop 1
	v_addc_co_u32_e64 v13, s[6:7], 0, v13, s[4:5]
	s_and_b64 s[4:5], s[4:5], vcc
	v_addc_co_u32_e64 v14, s[4:5], 0, v14, s[4:5]
	v_cmp_eq_u32_e64 s[4:5], 3, v38
	s_nop 1
	v_addc_co_u32_e64 v11, s[6:7], 0, v11, s[4:5]
	s_and_b64 s[4:5], s[4:5], vcc
	v_addc_co_u32_e64 v12, s[4:5], 0, v12, s[4:5]
	v_cmp_eq_u32_e64 s[4:5], 4, v38
	s_nop 1
	v_addc_co_u32_e64 v9, s[6:7], 0, v9, s[4:5]
	s_and_b64 s[4:5], s[4:5], vcc
	v_addc_co_u32_e64 v10, s[4:5], 0, v10, s[4:5]
	v_cmp_eq_u32_e64 s[4:5], 5, v38
	s_nop 1
	v_addc_co_u32_e64 v7, s[6:7], 0, v7, s[4:5]
	s_and_b64 s[4:5], s[4:5], vcc
	v_addc_co_u32_e64 v8, s[4:5], 0, v8, s[4:5]
	v_cmp_eq_u32_e64 s[4:5], 6, v38
	s_nop 1
	v_addc_co_u32_e64 v5, s[6:7], 0, v5, s[4:5]
	s_and_b64 s[4:5], s[4:5], vcc
	v_addc_co_u32_e64 v6, s[4:5], 0, v6, s[4:5]
	v_cmp_eq_u32_e64 s[4:5], 7, v38
	s_and_b64 vcc, s[4:5], vcc
	v_addc_co_u32_e32 v4, vcc, 0, v4, vcc
	v_addc_co_u32_e64 v3, s[6:7], 0, v3, s[4:5]
	v_add_u32_e32 v20, 0x200, v20
	v_cmp_gt_i32_e32 vcc, s17, v20
	s_waitcnt vmcnt(24)
	v_cmp_eq_u32_e64 s[4:5], 0, v39
	s_nop 1
	v_addc_co_u32_e64 v18, s[6:7], 0, v18, s[4:5]
	s_and_b64 s[4:5], s[4:5], vcc
	v_addc_co_u32_e64 v19, s[4:5], 0, v19, s[4:5]
	v_cmp_eq_u32_e64 s[4:5], 1, v39
	s_nop 1
	v_addc_co_u32_e64 v15, s[6:7], 0, v15, s[4:5]
	s_and_b64 s[4:5], s[4:5], vcc
	v_addc_co_u32_e64 v16, s[4:5], 0, v16, s[4:5]
	v_cmp_eq_u32_e64 s[4:5], 2, v39
	s_nop 1
	v_addc_co_u32_e64 v13, s[6:7], 0, v13, s[4:5]
	s_and_b64 s[4:5], s[4:5], vcc
	v_addc_co_u32_e64 v14, s[4:5], 0, v14, s[4:5]
	v_cmp_eq_u32_e64 s[4:5], 3, v39
	s_nop 1
	v_addc_co_u32_e64 v11, s[6:7], 0, v11, s[4:5]
	s_and_b64 s[4:5], s[4:5], vcc
	v_addc_co_u32_e64 v12, s[4:5], 0, v12, s[4:5]
	v_cmp_eq_u32_e64 s[4:5], 4, v39
	s_nop 1
	v_addc_co_u32_e64 v9, s[6:7], 0, v9, s[4:5]
	s_and_b64 s[4:5], s[4:5], vcc
	v_addc_co_u32_e64 v10, s[4:5], 0, v10, s[4:5]
	v_cmp_eq_u32_e64 s[4:5], 5, v39
	s_nop 1
	v_addc_co_u32_e64 v7, s[6:7], 0, v7, s[4:5]
	s_and_b64 s[4:5], s[4:5], vcc
	v_addc_co_u32_e64 v8, s[4:5], 0, v8, s[4:5]
	v_cmp_eq_u32_e64 s[4:5], 6, v39
	s_nop 1
	v_addc_co_u32_e64 v5, s[6:7], 0, v5, s[4:5]
	s_and_b64 s[4:5], s[4:5], vcc
	v_addc_co_u32_e64 v6, s[4:5], 0, v6, s[4:5]
	v_cmp_eq_u32_e64 s[4:5], 7, v39
	s_and_b64 vcc, s[4:5], vcc
	v_addc_co_u32_e32 v4, vcc, 0, v4, vcc
	v_addc_co_u32_e64 v3, s[6:7], 0, v3, s[4:5]
	v_add_u32_e32 v20, 0x200, v20
	v_cmp_gt_i32_e32 vcc, s17, v20
	s_waitcnt vmcnt(23)
	v_cmp_eq_u32_e64 s[4:5], 0, v40
	s_nop 1
	v_addc_co_u32_e64 v18, s[6:7], 0, v18, s[4:5]
	s_and_b64 s[4:5], s[4:5], vcc
	v_addc_co_u32_e64 v19, s[4:5], 0, v19, s[4:5]
	v_cmp_eq_u32_e64 s[4:5], 1, v40
	s_nop 1
	v_addc_co_u32_e64 v15, s[6:7], 0, v15, s[4:5]
	s_and_b64 s[4:5], s[4:5], vcc
	v_addc_co_u32_e64 v16, s[4:5], 0, v16, s[4:5]
	v_cmp_eq_u32_e64 s[4:5], 2, v40
	s_nop 1
	v_addc_co_u32_e64 v13, s[6:7], 0, v13, s[4:5]
	s_and_b64 s[4:5], s[4:5], vcc
	v_addc_co_u32_e64 v14, s[4:5], 0, v14, s[4:5]
	v_cmp_eq_u32_e64 s[4:5], 3, v40
	s_nop 1
	v_addc_co_u32_e64 v11, s[6:7], 0, v11, s[4:5]
	s_and_b64 s[4:5], s[4:5], vcc
	v_addc_co_u32_e64 v12, s[4:5], 0, v12, s[4:5]
	v_cmp_eq_u32_e64 s[4:5], 4, v40
	s_nop 1
	v_addc_co_u32_e64 v9, s[6:7], 0, v9, s[4:5]
	s_and_b64 s[4:5], s[4:5], vcc
	v_addc_co_u32_e64 v10, s[4:5], 0, v10, s[4:5]
	v_cmp_eq_u32_e64 s[4:5], 5, v40
	s_nop 1
	v_addc_co_u32_e64 v7, s[6:7], 0, v7, s[4:5]
	s_and_b64 s[4:5], s[4:5], vcc
	v_addc_co_u32_e64 v8, s[4:5], 0, v8, s[4:5]
	v_cmp_eq_u32_e64 s[4:5], 6, v40
	s_nop 1
	v_addc_co_u32_e64 v5, s[6:7], 0, v5, s[4:5]
	s_and_b64 s[4:5], s[4:5], vcc
	v_addc_co_u32_e64 v6, s[4:5], 0, v6, s[4:5]
	v_cmp_eq_u32_e64 s[4:5], 7, v40
	s_and_b64 vcc, s[4:5], vcc
	v_addc_co_u32_e32 v4, vcc, 0, v4, vcc
	v_addc_co_u32_e64 v3, s[6:7], 0, v3, s[4:5]
	v_add_u32_e32 v20, 0x200, v20
	v_cmp_gt_i32_e32 vcc, s17, v20
	s_waitcnt vmcnt(22)
	v_cmp_eq_u32_e64 s[4:5], 0, v41
	s_nop 1
	v_addc_co_u32_e64 v18, s[6:7], 0, v18, s[4:5]
	s_and_b64 s[4:5], s[4:5], vcc
	v_addc_co_u32_e64 v19, s[4:5], 0, v19, s[4:5]
	v_cmp_eq_u32_e64 s[4:5], 1, v41
	s_nop 1
	v_addc_co_u32_e64 v15, s[6:7], 0, v15, s[4:5]
	s_and_b64 s[4:5], s[4:5], vcc
	v_addc_co_u32_e64 v16, s[4:5], 0, v16, s[4:5]
	v_cmp_eq_u32_e64 s[4:5], 2, v41
	s_nop 1
	v_addc_co_u32_e64 v13, s[6:7], 0, v13, s[4:5]
	s_and_b64 s[4:5], s[4:5], vcc
	v_addc_co_u32_e64 v14, s[4:5], 0, v14, s[4:5]
	v_cmp_eq_u32_e64 s[4:5], 3, v41
	s_nop 1
	v_addc_co_u32_e64 v11, s[6:7], 0, v11, s[4:5]
	s_and_b64 s[4:5], s[4:5], vcc
	v_addc_co_u32_e64 v12, s[4:5], 0, v12, s[4:5]
	v_cmp_eq_u32_e64 s[4:5], 4, v41
	s_nop 1
	v_addc_co_u32_e64 v9, s[6:7], 0, v9, s[4:5]
	s_and_b64 s[4:5], s[4:5], vcc
	v_addc_co_u32_e64 v10, s[4:5], 0, v10, s[4:5]
	v_cmp_eq_u32_e64 s[4:5], 5, v41
	s_nop 1
	v_addc_co_u32_e64 v7, s[6:7], 0, v7, s[4:5]
	s_and_b64 s[4:5], s[4:5], vcc
	v_addc_co_u32_e64 v8, s[4:5], 0, v8, s[4:5]
	v_cmp_eq_u32_e64 s[4:5], 6, v41
	s_nop 1
	v_addc_co_u32_e64 v5, s[6:7], 0, v5, s[4:5]
	s_and_b64 s[4:5], s[4:5], vcc
	v_addc_co_u32_e64 v6, s[4:5], 0, v6, s[4:5]
	v_cmp_eq_u32_e64 s[4:5], 7, v41
	s_and_b64 vcc, s[4:5], vcc
	v_addc_co_u32_e32 v4, vcc, 0, v4, vcc
	v_addc_co_u32_e64 v3, s[6:7], 0, v3, s[4:5]
	v_add_u32_e32 v20, 0x200, v20
	v_cmp_gt_i32_e32 vcc, s17, v20
	s_waitcnt vmcnt(21)
	v_cmp_eq_u32_e64 s[4:5], 0, v42
	s_nop 1
	v_addc_co_u32_e64 v18, s[6:7], 0, v18, s[4:5]
	s_and_b64 s[4:5], s[4:5], vcc
	v_addc_co_u32_e64 v19, s[4:5], 0, v19, s[4:5]
	v_cmp_eq_u32_e64 s[4:5], 1, v42
	s_nop 1
	v_addc_co_u32_e64 v15, s[6:7], 0, v15, s[4:5]
	s_and_b64 s[4:5], s[4:5], vcc
	v_addc_co_u32_e64 v16, s[4:5], 0, v16, s[4:5]
	v_cmp_eq_u32_e64 s[4:5], 2, v42
	s_nop 1
	v_addc_co_u32_e64 v13, s[6:7], 0, v13, s[4:5]
	s_and_b64 s[4:5], s[4:5], vcc
	v_addc_co_u32_e64 v14, s[4:5], 0, v14, s[4:5]
	v_cmp_eq_u32_e64 s[4:5], 3, v42
	s_nop 1
	v_addc_co_u32_e64 v11, s[6:7], 0, v11, s[4:5]
	s_and_b64 s[4:5], s[4:5], vcc
	v_addc_co_u32_e64 v12, s[4:5], 0, v12, s[4:5]
	v_cmp_eq_u32_e64 s[4:5], 4, v42
	s_nop 1
	v_addc_co_u32_e64 v9, s[6:7], 0, v9, s[4:5]
	s_and_b64 s[4:5], s[4:5], vcc
	v_addc_co_u32_e64 v10, s[4:5], 0, v10, s[4:5]
	v_cmp_eq_u32_e64 s[4:5], 5, v42
	s_nop 1
	v_addc_co_u32_e64 v7, s[6:7], 0, v7, s[4:5]
	s_and_b64 s[4:5], s[4:5], vcc
	v_addc_co_u32_e64 v8, s[4:5], 0, v8, s[4:5]
	v_cmp_eq_u32_e64 s[4:5], 6, v42
	s_nop 1
	v_addc_co_u32_e64 v5, s[6:7], 0, v5, s[4:5]
	s_and_b64 s[4:5], s[4:5], vcc
	v_addc_co_u32_e64 v6, s[4:5], 0, v6, s[4:5]
	v_cmp_eq_u32_e64 s[4:5], 7, v42
	s_and_b64 vcc, s[4:5], vcc
	v_addc_co_u32_e32 v4, vcc, 0, v4, vcc
	v_addc_co_u32_e64 v3, s[6:7], 0, v3, s[4:5]
	v_add_u32_e32 v20, 0x200, v20
	v_cmp_gt_i32_e32 vcc, s17, v20
	s_waitcnt vmcnt(20)
	v_cmp_eq_u32_e64 s[4:5], 0, v43
	s_nop 1
	v_addc_co_u32_e64 v18, s[6:7], 0, v18, s[4:5]
	s_and_b64 s[4:5], s[4:5], vcc
	v_addc_co_u32_e64 v19, s[4:5], 0, v19, s[4:5]
	v_cmp_eq_u32_e64 s[4:5], 1, v43
	s_nop 1
	v_addc_co_u32_e64 v15, s[6:7], 0, v15, s[4:5]
	s_and_b64 s[4:5], s[4:5], vcc
	v_addc_co_u32_e64 v16, s[4:5], 0, v16, s[4:5]
	v_cmp_eq_u32_e64 s[4:5], 2, v43
	s_nop 1
	v_addc_co_u32_e64 v13, s[6:7], 0, v13, s[4:5]
	s_and_b64 s[4:5], s[4:5], vcc
	v_addc_co_u32_e64 v14, s[4:5], 0, v14, s[4:5]
	v_cmp_eq_u32_e64 s[4:5], 3, v43
	s_nop 1
	v_addc_co_u32_e64 v11, s[6:7], 0, v11, s[4:5]
	s_and_b64 s[4:5], s[4:5], vcc
	v_addc_co_u32_e64 v12, s[4:5], 0, v12, s[4:5]
	v_cmp_eq_u32_e64 s[4:5], 4, v43
	s_nop 1
	v_addc_co_u32_e64 v9, s[6:7], 0, v9, s[4:5]
	s_and_b64 s[4:5], s[4:5], vcc
	v_addc_co_u32_e64 v10, s[4:5], 0, v10, s[4:5]
	v_cmp_eq_u32_e64 s[4:5], 5, v43
	s_nop 1
	v_addc_co_u32_e64 v7, s[6:7], 0, v7, s[4:5]
	s_and_b64 s[4:5], s[4:5], vcc
	v_addc_co_u32_e64 v8, s[4:5], 0, v8, s[4:5]
	v_cmp_eq_u32_e64 s[4:5], 6, v43
	s_nop 1
	v_addc_co_u32_e64 v5, s[6:7], 0, v5, s[4:5]
	s_and_b64 s[4:5], s[4:5], vcc
	v_addc_co_u32_e64 v6, s[4:5], 0, v6, s[4:5]
	v_cmp_eq_u32_e64 s[4:5], 7, v43
	s_and_b64 vcc, s[4:5], vcc
	v_addc_co_u32_e32 v4, vcc, 0, v4, vcc
	v_addc_co_u32_e64 v3, s[6:7], 0, v3, s[4:5]
	v_add_u32_e32 v20, 0x200, v20
	v_cmp_gt_i32_e32 vcc, s17, v20
	s_waitcnt vmcnt(19)
	v_cmp_eq_u32_e64 s[4:5], 0, v44
	s_nop 1
	v_addc_co_u32_e64 v18, s[6:7], 0, v18, s[4:5]
	s_and_b64 s[4:5], s[4:5], vcc
	v_addc_co_u32_e64 v19, s[4:5], 0, v19, s[4:5]
	v_cmp_eq_u32_e64 s[4:5], 1, v44
	s_nop 1
	v_addc_co_u32_e64 v15, s[6:7], 0, v15, s[4:5]
	s_and_b64 s[4:5], s[4:5], vcc
	v_addc_co_u32_e64 v16, s[4:5], 0, v16, s[4:5]
	v_cmp_eq_u32_e64 s[4:5], 2, v44
	s_nop 1
	v_addc_co_u32_e64 v13, s[6:7], 0, v13, s[4:5]
	s_and_b64 s[4:5], s[4:5], vcc
	v_addc_co_u32_e64 v14, s[4:5], 0, v14, s[4:5]
	v_cmp_eq_u32_e64 s[4:5], 3, v44
	s_nop 1
	v_addc_co_u32_e64 v11, s[6:7], 0, v11, s[4:5]
	s_and_b64 s[4:5], s[4:5], vcc
	v_addc_co_u32_e64 v12, s[4:5], 0, v12, s[4:5]
	v_cmp_eq_u32_e64 s[4:5], 4, v44
	s_nop 1
	v_addc_co_u32_e64 v9, s[6:7], 0, v9, s[4:5]
	s_and_b64 s[4:5], s[4:5], vcc
	v_addc_co_u32_e64 v10, s[4:5], 0, v10, s[4:5]
	v_cmp_eq_u32_e64 s[4:5], 5, v44
	s_nop 1
	v_addc_co_u32_e64 v7, s[6:7], 0, v7, s[4:5]
	s_and_b64 s[4:5], s[4:5], vcc
	v_addc_co_u32_e64 v8, s[4:5], 0, v8, s[4:5]
	v_cmp_eq_u32_e64 s[4:5], 6, v44
	s_nop 1
	v_addc_co_u32_e64 v5, s[6:7], 0, v5, s[4:5]
	s_and_b64 s[4:5], s[4:5], vcc
	v_addc_co_u32_e64 v6, s[4:5], 0, v6, s[4:5]
	v_cmp_eq_u32_e64 s[4:5], 7, v44
	s_and_b64 vcc, s[4:5], vcc
	v_addc_co_u32_e32 v4, vcc, 0, v4, vcc
	v_addc_co_u32_e64 v3, s[6:7], 0, v3, s[4:5]
	v_add_u32_e32 v20, 0x200, v20
	v_cmp_gt_i32_e32 vcc, s17, v20
	s_waitcnt vmcnt(18)
	v_cmp_eq_u32_e64 s[4:5], 0, v45
	s_nop 1
	v_addc_co_u32_e64 v18, s[6:7], 0, v18, s[4:5]
	s_and_b64 s[4:5], s[4:5], vcc
	v_addc_co_u32_e64 v19, s[4:5], 0, v19, s[4:5]
	v_cmp_eq_u32_e64 s[4:5], 1, v45
	s_nop 1
	v_addc_co_u32_e64 v15, s[6:7], 0, v15, s[4:5]
	s_and_b64 s[4:5], s[4:5], vcc
	v_addc_co_u32_e64 v16, s[4:5], 0, v16, s[4:5]
	v_cmp_eq_u32_e64 s[4:5], 2, v45
	s_nop 1
	v_addc_co_u32_e64 v13, s[6:7], 0, v13, s[4:5]
	s_and_b64 s[4:5], s[4:5], vcc
	v_addc_co_u32_e64 v14, s[4:5], 0, v14, s[4:5]
	v_cmp_eq_u32_e64 s[4:5], 3, v45
	s_nop 1
	v_addc_co_u32_e64 v11, s[6:7], 0, v11, s[4:5]
	s_and_b64 s[4:5], s[4:5], vcc
	v_addc_co_u32_e64 v12, s[4:5], 0, v12, s[4:5]
	v_cmp_eq_u32_e64 s[4:5], 4, v45
	s_nop 1
	v_addc_co_u32_e64 v9, s[6:7], 0, v9, s[4:5]
	s_and_b64 s[4:5], s[4:5], vcc
	v_addc_co_u32_e64 v10, s[4:5], 0, v10, s[4:5]
	v_cmp_eq_u32_e64 s[4:5], 5, v45
	s_nop 1
	v_addc_co_u32_e64 v7, s[6:7], 0, v7, s[4:5]
	s_and_b64 s[4:5], s[4:5], vcc
	v_addc_co_u32_e64 v8, s[4:5], 0, v8, s[4:5]
	v_cmp_eq_u32_e64 s[4:5], 6, v45
	s_nop 1
	v_addc_co_u32_e64 v5, s[6:7], 0, v5, s[4:5]
	s_and_b64 s[4:5], s[4:5], vcc
	v_addc_co_u32_e64 v6, s[4:5], 0, v6, s[4:5]
	v_cmp_eq_u32_e64 s[4:5], 7, v45
	s_and_b64 vcc, s[4:5], vcc
	v_addc_co_u32_e32 v4, vcc, 0, v4, vcc
	v_addc_co_u32_e64 v3, s[6:7], 0, v3, s[4:5]
	v_add_u32_e32 v20, 0x200, v20
	v_cmp_gt_i32_e32 vcc, s17, v20
	s_waitcnt vmcnt(17)
	v_cmp_eq_u32_e64 s[4:5], 0, v46
	s_nop 1
	v_addc_co_u32_e64 v18, s[6:7], 0, v18, s[4:5]
	s_and_b64 s[4:5], s[4:5], vcc
	v_addc_co_u32_e64 v19, s[4:5], 0, v19, s[4:5]
	v_cmp_eq_u32_e64 s[4:5], 1, v46
	s_nop 1
	v_addc_co_u32_e64 v15, s[6:7], 0, v15, s[4:5]
	s_and_b64 s[4:5], s[4:5], vcc
	v_addc_co_u32_e64 v16, s[4:5], 0, v16, s[4:5]
	v_cmp_eq_u32_e64 s[4:5], 2, v46
	s_nop 1
	v_addc_co_u32_e64 v13, s[6:7], 0, v13, s[4:5]
	s_and_b64 s[4:5], s[4:5], vcc
	v_addc_co_u32_e64 v14, s[4:5], 0, v14, s[4:5]
	v_cmp_eq_u32_e64 s[4:5], 3, v46
	s_nop 1
	v_addc_co_u32_e64 v11, s[6:7], 0, v11, s[4:5]
	s_and_b64 s[4:5], s[4:5], vcc
	v_addc_co_u32_e64 v12, s[4:5], 0, v12, s[4:5]
	v_cmp_eq_u32_e64 s[4:5], 4, v46
	s_nop 1
	v_addc_co_u32_e64 v9, s[6:7], 0, v9, s[4:5]
	s_and_b64 s[4:5], s[4:5], vcc
	v_addc_co_u32_e64 v10, s[4:5], 0, v10, s[4:5]
	v_cmp_eq_u32_e64 s[4:5], 5, v46
	s_nop 1
	v_addc_co_u32_e64 v7, s[6:7], 0, v7, s[4:5]
	s_and_b64 s[4:5], s[4:5], vcc
	v_addc_co_u32_e64 v8, s[4:5], 0, v8, s[4:5]
	v_cmp_eq_u32_e64 s[4:5], 6, v46
	s_nop 1
	v_addc_co_u32_e64 v5, s[6:7], 0, v5, s[4:5]
	s_and_b64 s[4:5], s[4:5], vcc
	v_addc_co_u32_e64 v6, s[4:5], 0, v6, s[4:5]
	v_cmp_eq_u32_e64 s[4:5], 7, v46
	s_and_b64 vcc, s[4:5], vcc
	v_addc_co_u32_e32 v4, vcc, 0, v4, vcc
	v_addc_co_u32_e64 v3, s[6:7], 0, v3, s[4:5]
	v_add_u32_e32 v20, 0x200, v20
	v_cmp_gt_i32_e32 vcc, s17, v20
	s_waitcnt vmcnt(16)
	v_cmp_eq_u32_e64 s[4:5], 0, v47
	s_nop 1
	v_addc_co_u32_e64 v18, s[6:7], 0, v18, s[4:5]
	s_and_b64 s[4:5], s[4:5], vcc
	v_addc_co_u32_e64 v19, s[4:5], 0, v19, s[4:5]
	v_cmp_eq_u32_e64 s[4:5], 1, v47
	s_nop 1
	v_addc_co_u32_e64 v15, s[6:7], 0, v15, s[4:5]
	s_and_b64 s[4:5], s[4:5], vcc
	v_addc_co_u32_e64 v16, s[4:5], 0, v16, s[4:5]
	v_cmp_eq_u32_e64 s[4:5], 2, v47
	s_nop 1
	v_addc_co_u32_e64 v13, s[6:7], 0, v13, s[4:5]
	s_and_b64 s[4:5], s[4:5], vcc
	v_addc_co_u32_e64 v14, s[4:5], 0, v14, s[4:5]
	v_cmp_eq_u32_e64 s[4:5], 3, v47
	s_nop 1
	v_addc_co_u32_e64 v11, s[6:7], 0, v11, s[4:5]
	s_and_b64 s[4:5], s[4:5], vcc
	v_addc_co_u32_e64 v12, s[4:5], 0, v12, s[4:5]
	v_cmp_eq_u32_e64 s[4:5], 4, v47
	s_nop 1
	v_addc_co_u32_e64 v9, s[6:7], 0, v9, s[4:5]
	s_and_b64 s[4:5], s[4:5], vcc
	v_addc_co_u32_e64 v10, s[4:5], 0, v10, s[4:5]
	v_cmp_eq_u32_e64 s[4:5], 5, v47
	s_nop 1
	v_addc_co_u32_e64 v7, s[6:7], 0, v7, s[4:5]
	s_and_b64 s[4:5], s[4:5], vcc
	v_addc_co_u32_e64 v8, s[4:5], 0, v8, s[4:5]
	v_cmp_eq_u32_e64 s[4:5], 6, v47
	s_nop 1
	v_addc_co_u32_e64 v5, s[6:7], 0, v5, s[4:5]
	s_and_b64 s[4:5], s[4:5], vcc
	v_addc_co_u32_e64 v6, s[4:5], 0, v6, s[4:5]
	v_cmp_eq_u32_e64 s[4:5], 7, v47
	s_and_b64 vcc, s[4:5], vcc
	v_addc_co_u32_e32 v4, vcc, 0, v4, vcc
	v_addc_co_u32_e64 v3, s[6:7], 0, v3, s[4:5]
	v_add_u32_e32 v20, 0x200, v20
	v_cmp_gt_i32_e32 vcc, s17, v20
	s_waitcnt vmcnt(15)
	v_cmp_eq_u32_e64 s[4:5], 0, v48
	s_nop 1
	v_addc_co_u32_e64 v18, s[6:7], 0, v18, s[4:5]
	s_and_b64 s[4:5], s[4:5], vcc
	v_addc_co_u32_e64 v19, s[4:5], 0, v19, s[4:5]
	v_cmp_eq_u32_e64 s[4:5], 1, v48
	s_nop 1
	v_addc_co_u32_e64 v15, s[6:7], 0, v15, s[4:5]
	s_and_b64 s[4:5], s[4:5], vcc
	v_addc_co_u32_e64 v16, s[4:5], 0, v16, s[4:5]
	v_cmp_eq_u32_e64 s[4:5], 2, v48
	s_nop 1
	v_addc_co_u32_e64 v13, s[6:7], 0, v13, s[4:5]
	s_and_b64 s[4:5], s[4:5], vcc
	v_addc_co_u32_e64 v14, s[4:5], 0, v14, s[4:5]
	v_cmp_eq_u32_e64 s[4:5], 3, v48
	s_nop 1
	v_addc_co_u32_e64 v11, s[6:7], 0, v11, s[4:5]
	s_and_b64 s[4:5], s[4:5], vcc
	v_addc_co_u32_e64 v12, s[4:5], 0, v12, s[4:5]
	v_cmp_eq_u32_e64 s[4:5], 4, v48
	s_nop 1
	v_addc_co_u32_e64 v9, s[6:7], 0, v9, s[4:5]
	s_and_b64 s[4:5], s[4:5], vcc
	v_addc_co_u32_e64 v10, s[4:5], 0, v10, s[4:5]
	v_cmp_eq_u32_e64 s[4:5], 5, v48
	s_nop 1
	v_addc_co_u32_e64 v7, s[6:7], 0, v7, s[4:5]
	s_and_b64 s[4:5], s[4:5], vcc
	v_addc_co_u32_e64 v8, s[4:5], 0, v8, s[4:5]
	v_cmp_eq_u32_e64 s[4:5], 6, v48
	s_nop 1
	v_addc_co_u32_e64 v5, s[6:7], 0, v5, s[4:5]
	s_and_b64 s[4:5], s[4:5], vcc
	v_addc_co_u32_e64 v6, s[4:5], 0, v6, s[4:5]
	v_cmp_eq_u32_e64 s[4:5], 7, v48
	s_and_b64 vcc, s[4:5], vcc
	v_addc_co_u32_e32 v4, vcc, 0, v4, vcc
	v_addc_co_u32_e64 v3, s[6:7], 0, v3, s[4:5]
	v_add_u32_e32 v20, 0x200, v20
	v_cmp_gt_i32_e32 vcc, s17, v20
	s_waitcnt vmcnt(14)
	v_cmp_eq_u32_e64 s[4:5], 0, v49
	s_nop 1
	v_addc_co_u32_e64 v18, s[6:7], 0, v18, s[4:5]
	s_and_b64 s[4:5], s[4:5], vcc
	v_addc_co_u32_e64 v19, s[4:5], 0, v19, s[4:5]
	v_cmp_eq_u32_e64 s[4:5], 1, v49
	s_nop 1
	v_addc_co_u32_e64 v15, s[6:7], 0, v15, s[4:5]
	s_and_b64 s[4:5], s[4:5], vcc
	v_addc_co_u32_e64 v16, s[4:5], 0, v16, s[4:5]
	v_cmp_eq_u32_e64 s[4:5], 2, v49
	s_nop 1
	v_addc_co_u32_e64 v13, s[6:7], 0, v13, s[4:5]
	s_and_b64 s[4:5], s[4:5], vcc
	v_addc_co_u32_e64 v14, s[4:5], 0, v14, s[4:5]
	v_cmp_eq_u32_e64 s[4:5], 3, v49
	s_nop 1
	v_addc_co_u32_e64 v11, s[6:7], 0, v11, s[4:5]
	s_and_b64 s[4:5], s[4:5], vcc
	v_addc_co_u32_e64 v12, s[4:5], 0, v12, s[4:5]
	v_cmp_eq_u32_e64 s[4:5], 4, v49
	s_nop 1
	v_addc_co_u32_e64 v9, s[6:7], 0, v9, s[4:5]
	s_and_b64 s[4:5], s[4:5], vcc
	v_addc_co_u32_e64 v10, s[4:5], 0, v10, s[4:5]
	v_cmp_eq_u32_e64 s[4:5], 5, v49
	s_nop 1
	v_addc_co_u32_e64 v7, s[6:7], 0, v7, s[4:5]
	s_and_b64 s[4:5], s[4:5], vcc
	v_addc_co_u32_e64 v8, s[4:5], 0, v8, s[4:5]
	v_cmp_eq_u32_e64 s[4:5], 6, v49
	s_nop 1
	v_addc_co_u32_e64 v5, s[6:7], 0, v5, s[4:5]
	s_and_b64 s[4:5], s[4:5], vcc
	v_addc_co_u32_e64 v6, s[4:5], 0, v6, s[4:5]
	v_cmp_eq_u32_e64 s[4:5], 7, v49
	s_and_b64 vcc, s[4:5], vcc
	v_addc_co_u32_e32 v4, vcc, 0, v4, vcc
	v_addc_co_u32_e64 v3, s[6:7], 0, v3, s[4:5]
	v_add_u32_e32 v20, 0x200, v20
	v_cmp_gt_i32_e32 vcc, s17, v20
	s_waitcnt vmcnt(13)
	v_cmp_eq_u32_e64 s[4:5], 0, v50
	s_nop 1
	v_addc_co_u32_e64 v18, s[6:7], 0, v18, s[4:5]
	s_and_b64 s[4:5], s[4:5], vcc
	v_addc_co_u32_e64 v19, s[4:5], 0, v19, s[4:5]
	v_cmp_eq_u32_e64 s[4:5], 1, v50
	s_nop 1
	v_addc_co_u32_e64 v15, s[6:7], 0, v15, s[4:5]
	s_and_b64 s[4:5], s[4:5], vcc
	v_addc_co_u32_e64 v16, s[4:5], 0, v16, s[4:5]
	v_cmp_eq_u32_e64 s[4:5], 2, v50
	s_nop 1
	v_addc_co_u32_e64 v13, s[6:7], 0, v13, s[4:5]
	s_and_b64 s[4:5], s[4:5], vcc
	v_addc_co_u32_e64 v14, s[4:5], 0, v14, s[4:5]
	v_cmp_eq_u32_e64 s[4:5], 3, v50
	s_nop 1
	v_addc_co_u32_e64 v11, s[6:7], 0, v11, s[4:5]
	s_and_b64 s[4:5], s[4:5], vcc
	v_addc_co_u32_e64 v12, s[4:5], 0, v12, s[4:5]
	v_cmp_eq_u32_e64 s[4:5], 4, v50
	s_nop 1
	v_addc_co_u32_e64 v9, s[6:7], 0, v9, s[4:5]
	s_and_b64 s[4:5], s[4:5], vcc
	v_addc_co_u32_e64 v10, s[4:5], 0, v10, s[4:5]
	v_cmp_eq_u32_e64 s[4:5], 5, v50
	s_nop 1
	v_addc_co_u32_e64 v7, s[6:7], 0, v7, s[4:5]
	s_and_b64 s[4:5], s[4:5], vcc
	v_addc_co_u32_e64 v8, s[4:5], 0, v8, s[4:5]
	v_cmp_eq_u32_e64 s[4:5], 6, v50
	s_nop 1
	v_addc_co_u32_e64 v5, s[6:7], 0, v5, s[4:5]
	s_and_b64 s[4:5], s[4:5], vcc
	v_addc_co_u32_e64 v6, s[4:5], 0, v6, s[4:5]
	v_cmp_eq_u32_e64 s[4:5], 7, v50
	s_and_b64 vcc, s[4:5], vcc
	v_addc_co_u32_e32 v4, vcc, 0, v4, vcc
	v_addc_co_u32_e64 v3, s[6:7], 0, v3, s[4:5]
	v_add_u32_e32 v20, 0x200, v20
	v_cmp_gt_i32_e32 vcc, s17, v20
	s_waitcnt vmcnt(12)
	v_cmp_eq_u32_e64 s[4:5], 0, v51
	s_nop 1
	v_addc_co_u32_e64 v18, s[6:7], 0, v18, s[4:5]
	s_and_b64 s[4:5], s[4:5], vcc
	v_addc_co_u32_e64 v19, s[4:5], 0, v19, s[4:5]
	v_cmp_eq_u32_e64 s[4:5], 1, v51
	s_nop 1
	v_addc_co_u32_e64 v15, s[6:7], 0, v15, s[4:5]
	s_and_b64 s[4:5], s[4:5], vcc
	v_addc_co_u32_e64 v16, s[4:5], 0, v16, s[4:5]
	v_cmp_eq_u32_e64 s[4:5], 2, v51
	s_nop 1
	v_addc_co_u32_e64 v13, s[6:7], 0, v13, s[4:5]
	s_and_b64 s[4:5], s[4:5], vcc
	v_addc_co_u32_e64 v14, s[4:5], 0, v14, s[4:5]
	v_cmp_eq_u32_e64 s[4:5], 3, v51
	s_nop 1
	v_addc_co_u32_e64 v11, s[6:7], 0, v11, s[4:5]
	s_and_b64 s[4:5], s[4:5], vcc
	v_addc_co_u32_e64 v12, s[4:5], 0, v12, s[4:5]
	v_cmp_eq_u32_e64 s[4:5], 4, v51
	s_nop 1
	v_addc_co_u32_e64 v9, s[6:7], 0, v9, s[4:5]
	s_and_b64 s[4:5], s[4:5], vcc
	v_addc_co_u32_e64 v10, s[4:5], 0, v10, s[4:5]
	v_cmp_eq_u32_e64 s[4:5], 5, v51
	s_nop 1
	v_addc_co_u32_e64 v7, s[6:7], 0, v7, s[4:5]
	s_and_b64 s[4:5], s[4:5], vcc
	v_addc_co_u32_e64 v8, s[4:5], 0, v8, s[4:5]
	v_cmp_eq_u32_e64 s[4:5], 6, v51
	s_nop 1
	v_addc_co_u32_e64 v5, s[6:7], 0, v5, s[4:5]
	s_and_b64 s[4:5], s[4:5], vcc
	v_addc_co_u32_e64 v6, s[4:5], 0, v6, s[4:5]
	v_cmp_eq_u32_e64 s[4:5], 7, v51
	s_and_b64 vcc, s[4:5], vcc
	v_addc_co_u32_e32 v4, vcc, 0, v4, vcc
	v_addc_co_u32_e64 v3, s[6:7], 0, v3, s[4:5]
	v_add_u32_e32 v20, 0x200, v20
	v_cmp_gt_i32_e32 vcc, s17, v20
	s_waitcnt vmcnt(11)
	v_cmp_eq_u32_e64 s[4:5], 0, v52
	s_nop 1
	v_addc_co_u32_e64 v18, s[6:7], 0, v18, s[4:5]
	s_and_b64 s[4:5], s[4:5], vcc
	v_addc_co_u32_e64 v19, s[4:5], 0, v19, s[4:5]
	v_cmp_eq_u32_e64 s[4:5], 1, v52
	s_nop 1
	v_addc_co_u32_e64 v15, s[6:7], 0, v15, s[4:5]
	s_and_b64 s[4:5], s[4:5], vcc
	v_addc_co_u32_e64 v16, s[4:5], 0, v16, s[4:5]
	v_cmp_eq_u32_e64 s[4:5], 2, v52
	s_nop 1
	v_addc_co_u32_e64 v13, s[6:7], 0, v13, s[4:5]
	s_and_b64 s[4:5], s[4:5], vcc
	v_addc_co_u32_e64 v14, s[4:5], 0, v14, s[4:5]
	v_cmp_eq_u32_e64 s[4:5], 3, v52
	s_nop 1
	v_addc_co_u32_e64 v11, s[6:7], 0, v11, s[4:5]
	s_and_b64 s[4:5], s[4:5], vcc
	v_addc_co_u32_e64 v12, s[4:5], 0, v12, s[4:5]
	v_cmp_eq_u32_e64 s[4:5], 4, v52
	s_nop 1
	v_addc_co_u32_e64 v9, s[6:7], 0, v9, s[4:5]
	s_and_b64 s[4:5], s[4:5], vcc
	v_addc_co_u32_e64 v10, s[4:5], 0, v10, s[4:5]
	v_cmp_eq_u32_e64 s[4:5], 5, v52
	s_nop 1
	v_addc_co_u32_e64 v7, s[6:7], 0, v7, s[4:5]
	s_and_b64 s[4:5], s[4:5], vcc
	v_addc_co_u32_e64 v8, s[4:5], 0, v8, s[4:5]
	v_cmp_eq_u32_e64 s[4:5], 6, v52
	s_nop 1
	v_addc_co_u32_e64 v5, s[6:7], 0, v5, s[4:5]
	s_and_b64 s[4:5], s[4:5], vcc
	v_addc_co_u32_e64 v6, s[4:5], 0, v6, s[4:5]
	v_cmp_eq_u32_e64 s[4:5], 7, v52
	s_and_b64 vcc, s[4:5], vcc
	v_addc_co_u32_e32 v4, vcc, 0, v4, vcc
	v_addc_co_u32_e64 v3, s[6:7], 0, v3, s[4:5]
	v_add_u32_e32 v20, 0x200, v20
	v_cmp_gt_i32_e32 vcc, s17, v20
	s_waitcnt vmcnt(10)
	v_cmp_eq_u32_e64 s[4:5], 0, v53
	s_nop 1
	v_addc_co_u32_e64 v18, s[6:7], 0, v18, s[4:5]
	s_and_b64 s[4:5], s[4:5], vcc
	v_addc_co_u32_e64 v19, s[4:5], 0, v19, s[4:5]
	v_cmp_eq_u32_e64 s[4:5], 1, v53
	s_nop 1
	v_addc_co_u32_e64 v15, s[6:7], 0, v15, s[4:5]
	s_and_b64 s[4:5], s[4:5], vcc
	v_addc_co_u32_e64 v16, s[4:5], 0, v16, s[4:5]
	v_cmp_eq_u32_e64 s[4:5], 2, v53
	s_nop 1
	v_addc_co_u32_e64 v13, s[6:7], 0, v13, s[4:5]
	s_and_b64 s[4:5], s[4:5], vcc
	v_addc_co_u32_e64 v14, s[4:5], 0, v14, s[4:5]
	v_cmp_eq_u32_e64 s[4:5], 3, v53
	s_nop 1
	v_addc_co_u32_e64 v11, s[6:7], 0, v11, s[4:5]
	s_and_b64 s[4:5], s[4:5], vcc
	v_addc_co_u32_e64 v12, s[4:5], 0, v12, s[4:5]
	v_cmp_eq_u32_e64 s[4:5], 4, v53
	s_nop 1
	v_addc_co_u32_e64 v9, s[6:7], 0, v9, s[4:5]
	s_and_b64 s[4:5], s[4:5], vcc
	v_addc_co_u32_e64 v10, s[4:5], 0, v10, s[4:5]
	v_cmp_eq_u32_e64 s[4:5], 5, v53
	s_nop 1
	v_addc_co_u32_e64 v7, s[6:7], 0, v7, s[4:5]
	s_and_b64 s[4:5], s[4:5], vcc
	v_addc_co_u32_e64 v8, s[4:5], 0, v8, s[4:5]
	v_cmp_eq_u32_e64 s[4:5], 6, v53
	s_nop 1
	v_addc_co_u32_e64 v5, s[6:7], 0, v5, s[4:5]
	s_and_b64 s[4:5], s[4:5], vcc
	v_addc_co_u32_e64 v6, s[4:5], 0, v6, s[4:5]
	v_cmp_eq_u32_e64 s[4:5], 7, v53
	s_and_b64 vcc, s[4:5], vcc
	v_addc_co_u32_e32 v4, vcc, 0, v4, vcc
	v_addc_co_u32_e64 v3, s[6:7], 0, v3, s[4:5]
	v_add_u32_e32 v20, 0x200, v20
	v_cmp_gt_i32_e32 vcc, s17, v20
	s_waitcnt vmcnt(9)
	v_cmp_eq_u32_e64 s[4:5], 0, v54
	s_nop 1
	v_addc_co_u32_e64 v18, s[6:7], 0, v18, s[4:5]
	s_and_b64 s[4:5], s[4:5], vcc
	v_addc_co_u32_e64 v19, s[4:5], 0, v19, s[4:5]
	v_cmp_eq_u32_e64 s[4:5], 1, v54
	s_nop 1
	v_addc_co_u32_e64 v15, s[6:7], 0, v15, s[4:5]
	s_and_b64 s[4:5], s[4:5], vcc
	v_addc_co_u32_e64 v16, s[4:5], 0, v16, s[4:5]
	v_cmp_eq_u32_e64 s[4:5], 2, v54
	s_nop 1
	v_addc_co_u32_e64 v13, s[6:7], 0, v13, s[4:5]
	s_and_b64 s[4:5], s[4:5], vcc
	v_addc_co_u32_e64 v14, s[4:5], 0, v14, s[4:5]
	v_cmp_eq_u32_e64 s[4:5], 3, v54
	s_nop 1
	v_addc_co_u32_e64 v11, s[6:7], 0, v11, s[4:5]
	s_and_b64 s[4:5], s[4:5], vcc
	v_addc_co_u32_e64 v12, s[4:5], 0, v12, s[4:5]
	v_cmp_eq_u32_e64 s[4:5], 4, v54
	s_nop 1
	v_addc_co_u32_e64 v9, s[6:7], 0, v9, s[4:5]
	s_and_b64 s[4:5], s[4:5], vcc
	v_addc_co_u32_e64 v10, s[4:5], 0, v10, s[4:5]
	v_cmp_eq_u32_e64 s[4:5], 5, v54
	s_nop 1
	v_addc_co_u32_e64 v7, s[6:7], 0, v7, s[4:5]
	s_and_b64 s[4:5], s[4:5], vcc
	v_addc_co_u32_e64 v8, s[4:5], 0, v8, s[4:5]
	v_cmp_eq_u32_e64 s[4:5], 6, v54
	s_nop 1
	v_addc_co_u32_e64 v5, s[6:7], 0, v5, s[4:5]
	s_and_b64 s[4:5], s[4:5], vcc
	v_addc_co_u32_e64 v6, s[4:5], 0, v6, s[4:5]
	v_cmp_eq_u32_e64 s[4:5], 7, v54
	s_and_b64 vcc, s[4:5], vcc
	v_addc_co_u32_e32 v4, vcc, 0, v4, vcc
	v_addc_co_u32_e64 v3, s[6:7], 0, v3, s[4:5]
	v_add_u32_e32 v20, 0x200, v20
	v_cmp_gt_i32_e32 vcc, s17, v20
	s_waitcnt vmcnt(8)
	v_cmp_eq_u32_e64 s[4:5], 0, v55
	s_nop 1
	v_addc_co_u32_e64 v18, s[6:7], 0, v18, s[4:5]
	s_and_b64 s[4:5], s[4:5], vcc
	v_addc_co_u32_e64 v19, s[4:5], 0, v19, s[4:5]
	v_cmp_eq_u32_e64 s[4:5], 1, v55
	s_nop 1
	v_addc_co_u32_e64 v15, s[6:7], 0, v15, s[4:5]
	s_and_b64 s[4:5], s[4:5], vcc
	v_addc_co_u32_e64 v16, s[4:5], 0, v16, s[4:5]
	v_cmp_eq_u32_e64 s[4:5], 2, v55
	s_nop 1
	v_addc_co_u32_e64 v13, s[6:7], 0, v13, s[4:5]
	s_and_b64 s[4:5], s[4:5], vcc
	v_addc_co_u32_e64 v14, s[4:5], 0, v14, s[4:5]
	v_cmp_eq_u32_e64 s[4:5], 3, v55
	s_nop 1
	v_addc_co_u32_e64 v11, s[6:7], 0, v11, s[4:5]
	s_and_b64 s[4:5], s[4:5], vcc
	v_addc_co_u32_e64 v12, s[4:5], 0, v12, s[4:5]
	v_cmp_eq_u32_e64 s[4:5], 4, v55
	s_nop 1
	v_addc_co_u32_e64 v9, s[6:7], 0, v9, s[4:5]
	s_and_b64 s[4:5], s[4:5], vcc
	v_addc_co_u32_e64 v10, s[4:5], 0, v10, s[4:5]
	v_cmp_eq_u32_e64 s[4:5], 5, v55
	s_nop 1
	v_addc_co_u32_e64 v7, s[6:7], 0, v7, s[4:5]
	s_and_b64 s[4:5], s[4:5], vcc
	v_addc_co_u32_e64 v8, s[4:5], 0, v8, s[4:5]
	v_cmp_eq_u32_e64 s[4:5], 6, v55
	s_nop 1
	v_addc_co_u32_e64 v5, s[6:7], 0, v5, s[4:5]
	s_and_b64 s[4:5], s[4:5], vcc
	v_addc_co_u32_e64 v6, s[4:5], 0, v6, s[4:5]
	v_cmp_eq_u32_e64 s[4:5], 7, v55
	s_and_b64 vcc, s[4:5], vcc
	v_addc_co_u32_e32 v4, vcc, 0, v4, vcc
	v_addc_co_u32_e64 v3, s[6:7], 0, v3, s[4:5]
	v_add_u32_e32 v20, 0x200, v20
	v_cmp_gt_i32_e32 vcc, s17, v20
	s_waitcnt vmcnt(7)
	v_cmp_eq_u32_e64 s[4:5], 0, v56
	s_nop 1
	v_addc_co_u32_e64 v18, s[6:7], 0, v18, s[4:5]
	s_and_b64 s[4:5], s[4:5], vcc
	v_addc_co_u32_e64 v19, s[4:5], 0, v19, s[4:5]
	v_cmp_eq_u32_e64 s[4:5], 1, v56
	s_nop 1
	v_addc_co_u32_e64 v15, s[6:7], 0, v15, s[4:5]
	s_and_b64 s[4:5], s[4:5], vcc
	v_addc_co_u32_e64 v16, s[4:5], 0, v16, s[4:5]
	v_cmp_eq_u32_e64 s[4:5], 2, v56
	s_nop 1
	v_addc_co_u32_e64 v13, s[6:7], 0, v13, s[4:5]
	s_and_b64 s[4:5], s[4:5], vcc
	v_addc_co_u32_e64 v14, s[4:5], 0, v14, s[4:5]
	v_cmp_eq_u32_e64 s[4:5], 3, v56
	s_nop 1
	v_addc_co_u32_e64 v11, s[6:7], 0, v11, s[4:5]
	s_and_b64 s[4:5], s[4:5], vcc
	v_addc_co_u32_e64 v12, s[4:5], 0, v12, s[4:5]
	v_cmp_eq_u32_e64 s[4:5], 4, v56
	s_nop 1
	v_addc_co_u32_e64 v9, s[6:7], 0, v9, s[4:5]
	s_and_b64 s[4:5], s[4:5], vcc
	v_addc_co_u32_e64 v10, s[4:5], 0, v10, s[4:5]
	v_cmp_eq_u32_e64 s[4:5], 5, v56
	s_nop 1
	v_addc_co_u32_e64 v7, s[6:7], 0, v7, s[4:5]
	s_and_b64 s[4:5], s[4:5], vcc
	v_addc_co_u32_e64 v8, s[4:5], 0, v8, s[4:5]
	v_cmp_eq_u32_e64 s[4:5], 6, v56
	s_nop 1
	v_addc_co_u32_e64 v5, s[6:7], 0, v5, s[4:5]
	s_and_b64 s[4:5], s[4:5], vcc
	v_addc_co_u32_e64 v6, s[4:5], 0, v6, s[4:5]
	v_cmp_eq_u32_e64 s[4:5], 7, v56
	s_and_b64 vcc, s[4:5], vcc
	v_addc_co_u32_e32 v4, vcc, 0, v4, vcc
	v_addc_co_u32_e64 v3, s[6:7], 0, v3, s[4:5]
	v_add_u32_e32 v20, 0x200, v20
	v_cmp_gt_i32_e32 vcc, s17, v20
	s_waitcnt vmcnt(6)
	v_cmp_eq_u32_e64 s[4:5], 0, v57
	s_nop 1
	v_addc_co_u32_e64 v18, s[6:7], 0, v18, s[4:5]
	s_and_b64 s[4:5], s[4:5], vcc
	v_addc_co_u32_e64 v19, s[4:5], 0, v19, s[4:5]
	v_cmp_eq_u32_e64 s[4:5], 1, v57
	s_nop 1
	v_addc_co_u32_e64 v15, s[6:7], 0, v15, s[4:5]
	s_and_b64 s[4:5], s[4:5], vcc
	v_addc_co_u32_e64 v16, s[4:5], 0, v16, s[4:5]
	v_cmp_eq_u32_e64 s[4:5], 2, v57
	s_nop 1
	v_addc_co_u32_e64 v13, s[6:7], 0, v13, s[4:5]
	s_and_b64 s[4:5], s[4:5], vcc
	v_addc_co_u32_e64 v14, s[4:5], 0, v14, s[4:5]
	v_cmp_eq_u32_e64 s[4:5], 3, v57
	s_nop 1
	v_addc_co_u32_e64 v11, s[6:7], 0, v11, s[4:5]
	s_and_b64 s[4:5], s[4:5], vcc
	v_addc_co_u32_e64 v12, s[4:5], 0, v12, s[4:5]
	v_cmp_eq_u32_e64 s[4:5], 4, v57
	s_nop 1
	v_addc_co_u32_e64 v9, s[6:7], 0, v9, s[4:5]
	s_and_b64 s[4:5], s[4:5], vcc
	v_addc_co_u32_e64 v10, s[4:5], 0, v10, s[4:5]
	v_cmp_eq_u32_e64 s[4:5], 5, v57
	s_nop 1
	v_addc_co_u32_e64 v7, s[6:7], 0, v7, s[4:5]
	s_and_b64 s[4:5], s[4:5], vcc
	v_addc_co_u32_e64 v8, s[4:5], 0, v8, s[4:5]
	v_cmp_eq_u32_e64 s[4:5], 6, v57
	s_nop 1
	v_addc_co_u32_e64 v5, s[6:7], 0, v5, s[4:5]
	s_and_b64 s[4:5], s[4:5], vcc
	v_addc_co_u32_e64 v6, s[4:5], 0, v6, s[4:5]
	v_cmp_eq_u32_e64 s[4:5], 7, v57
	s_and_b64 vcc, s[4:5], vcc
	v_addc_co_u32_e32 v4, vcc, 0, v4, vcc
	v_addc_co_u32_e64 v3, s[6:7], 0, v3, s[4:5]
	v_add_u32_e32 v20, 0x200, v20
	v_cmp_gt_i32_e32 vcc, s17, v20
	s_waitcnt vmcnt(5)
	v_cmp_eq_u32_e64 s[4:5], 0, v58
	s_nop 1
	v_addc_co_u32_e64 v18, s[6:7], 0, v18, s[4:5]
	s_and_b64 s[4:5], s[4:5], vcc
	v_addc_co_u32_e64 v19, s[4:5], 0, v19, s[4:5]
	v_cmp_eq_u32_e64 s[4:5], 1, v58
	s_nop 1
	v_addc_co_u32_e64 v15, s[6:7], 0, v15, s[4:5]
	s_and_b64 s[4:5], s[4:5], vcc
	v_addc_co_u32_e64 v16, s[4:5], 0, v16, s[4:5]
	v_cmp_eq_u32_e64 s[4:5], 2, v58
	s_nop 1
	v_addc_co_u32_e64 v13, s[6:7], 0, v13, s[4:5]
	s_and_b64 s[4:5], s[4:5], vcc
	v_addc_co_u32_e64 v14, s[4:5], 0, v14, s[4:5]
	v_cmp_eq_u32_e64 s[4:5], 3, v58
	s_nop 1
	v_addc_co_u32_e64 v11, s[6:7], 0, v11, s[4:5]
	s_and_b64 s[4:5], s[4:5], vcc
	v_addc_co_u32_e64 v12, s[4:5], 0, v12, s[4:5]
	v_cmp_eq_u32_e64 s[4:5], 4, v58
	s_nop 1
	v_addc_co_u32_e64 v9, s[6:7], 0, v9, s[4:5]
	s_and_b64 s[4:5], s[4:5], vcc
	v_addc_co_u32_e64 v10, s[4:5], 0, v10, s[4:5]
	v_cmp_eq_u32_e64 s[4:5], 5, v58
	s_nop 1
	v_addc_co_u32_e64 v7, s[6:7], 0, v7, s[4:5]
	s_and_b64 s[4:5], s[4:5], vcc
	v_addc_co_u32_e64 v8, s[4:5], 0, v8, s[4:5]
	v_cmp_eq_u32_e64 s[4:5], 6, v58
	s_nop 1
	v_addc_co_u32_e64 v5, s[6:7], 0, v5, s[4:5]
	s_and_b64 s[4:5], s[4:5], vcc
	v_addc_co_u32_e64 v6, s[4:5], 0, v6, s[4:5]
	v_cmp_eq_u32_e64 s[4:5], 7, v58
	s_and_b64 vcc, s[4:5], vcc
	v_addc_co_u32_e32 v4, vcc, 0, v4, vcc
	v_addc_co_u32_e64 v3, s[6:7], 0, v3, s[4:5]
	v_add_u32_e32 v20, 0x200, v20
	v_cmp_gt_i32_e32 vcc, s17, v20
	s_waitcnt vmcnt(4)
	v_cmp_eq_u32_e64 s[4:5], 0, v59
	s_nop 1
	v_addc_co_u32_e64 v18, s[6:7], 0, v18, s[4:5]
	s_and_b64 s[4:5], s[4:5], vcc
	v_addc_co_u32_e64 v19, s[4:5], 0, v19, s[4:5]
	v_cmp_eq_u32_e64 s[4:5], 1, v59
	s_nop 1
	v_addc_co_u32_e64 v15, s[6:7], 0, v15, s[4:5]
	s_and_b64 s[4:5], s[4:5], vcc
	v_addc_co_u32_e64 v16, s[4:5], 0, v16, s[4:5]
	v_cmp_eq_u32_e64 s[4:5], 2, v59
	s_nop 1
	v_addc_co_u32_e64 v13, s[6:7], 0, v13, s[4:5]
	s_and_b64 s[4:5], s[4:5], vcc
	v_addc_co_u32_e64 v14, s[4:5], 0, v14, s[4:5]
	v_cmp_eq_u32_e64 s[4:5], 3, v59
	s_nop 1
	v_addc_co_u32_e64 v11, s[6:7], 0, v11, s[4:5]
	s_and_b64 s[4:5], s[4:5], vcc
	v_addc_co_u32_e64 v12, s[4:5], 0, v12, s[4:5]
	v_cmp_eq_u32_e64 s[4:5], 4, v59
	s_nop 1
	v_addc_co_u32_e64 v9, s[6:7], 0, v9, s[4:5]
	s_and_b64 s[4:5], s[4:5], vcc
	v_addc_co_u32_e64 v10, s[4:5], 0, v10, s[4:5]
	v_cmp_eq_u32_e64 s[4:5], 5, v59
	s_nop 1
	v_addc_co_u32_e64 v7, s[6:7], 0, v7, s[4:5]
	s_and_b64 s[4:5], s[4:5], vcc
	v_addc_co_u32_e64 v8, s[4:5], 0, v8, s[4:5]
	v_cmp_eq_u32_e64 s[4:5], 6, v59
	s_nop 1
	v_addc_co_u32_e64 v5, s[6:7], 0, v5, s[4:5]
	s_and_b64 s[4:5], s[4:5], vcc
	v_addc_co_u32_e64 v6, s[4:5], 0, v6, s[4:5]
	v_cmp_eq_u32_e64 s[4:5], 7, v59
	s_and_b64 vcc, s[4:5], vcc
	v_addc_co_u32_e32 v4, vcc, 0, v4, vcc
	v_addc_co_u32_e64 v3, s[6:7], 0, v3, s[4:5]
	v_add_u32_e32 v20, 0x200, v20
	v_cmp_gt_i32_e32 vcc, s17, v20
	s_waitcnt vmcnt(3)
	v_cmp_eq_u32_e64 s[4:5], 0, v60
	s_nop 1
	v_addc_co_u32_e64 v18, s[6:7], 0, v18, s[4:5]
	s_and_b64 s[4:5], s[4:5], vcc
	v_addc_co_u32_e64 v19, s[4:5], 0, v19, s[4:5]
	v_cmp_eq_u32_e64 s[4:5], 1, v60
	s_nop 1
	v_addc_co_u32_e64 v15, s[6:7], 0, v15, s[4:5]
	s_and_b64 s[4:5], s[4:5], vcc
	v_addc_co_u32_e64 v16, s[4:5], 0, v16, s[4:5]
	v_cmp_eq_u32_e64 s[4:5], 2, v60
	s_nop 1
	v_addc_co_u32_e64 v13, s[6:7], 0, v13, s[4:5]
	s_and_b64 s[4:5], s[4:5], vcc
	v_addc_co_u32_e64 v14, s[4:5], 0, v14, s[4:5]
	v_cmp_eq_u32_e64 s[4:5], 3, v60
	s_nop 1
	v_addc_co_u32_e64 v11, s[6:7], 0, v11, s[4:5]
	s_and_b64 s[4:5], s[4:5], vcc
	v_addc_co_u32_e64 v12, s[4:5], 0, v12, s[4:5]
	v_cmp_eq_u32_e64 s[4:5], 4, v60
	s_nop 1
	v_addc_co_u32_e64 v9, s[6:7], 0, v9, s[4:5]
	s_and_b64 s[4:5], s[4:5], vcc
	v_addc_co_u32_e64 v10, s[4:5], 0, v10, s[4:5]
	v_cmp_eq_u32_e64 s[4:5], 5, v60
	s_nop 1
	v_addc_co_u32_e64 v7, s[6:7], 0, v7, s[4:5]
	s_and_b64 s[4:5], s[4:5], vcc
	v_addc_co_u32_e64 v8, s[4:5], 0, v8, s[4:5]
	v_cmp_eq_u32_e64 s[4:5], 6, v60
	s_nop 1
	v_addc_co_u32_e64 v5, s[6:7], 0, v5, s[4:5]
	s_and_b64 s[4:5], s[4:5], vcc
	v_addc_co_u32_e64 v6, s[4:5], 0, v6, s[4:5]
	v_cmp_eq_u32_e64 s[4:5], 7, v60
	s_and_b64 vcc, s[4:5], vcc
	v_addc_co_u32_e32 v4, vcc, 0, v4, vcc
	v_addc_co_u32_e64 v3, s[6:7], 0, v3, s[4:5]
	v_add_u32_e32 v20, 0x200, v20
	v_cmp_gt_i32_e32 vcc, s17, v20
	s_waitcnt vmcnt(2)
	v_cmp_eq_u32_e64 s[4:5], 0, v61
	s_nop 1
	v_addc_co_u32_e64 v18, s[6:7], 0, v18, s[4:5]
	s_and_b64 s[4:5], s[4:5], vcc
	v_addc_co_u32_e64 v19, s[4:5], 0, v19, s[4:5]
	v_cmp_eq_u32_e64 s[4:5], 1, v61
	s_nop 1
	v_addc_co_u32_e64 v15, s[6:7], 0, v15, s[4:5]
	s_and_b64 s[4:5], s[4:5], vcc
	v_addc_co_u32_e64 v16, s[4:5], 0, v16, s[4:5]
	v_cmp_eq_u32_e64 s[4:5], 2, v61
	s_nop 1
	v_addc_co_u32_e64 v13, s[6:7], 0, v13, s[4:5]
	s_and_b64 s[4:5], s[4:5], vcc
	v_addc_co_u32_e64 v14, s[4:5], 0, v14, s[4:5]
	v_cmp_eq_u32_e64 s[4:5], 3, v61
	s_nop 1
	v_addc_co_u32_e64 v11, s[6:7], 0, v11, s[4:5]
	s_and_b64 s[4:5], s[4:5], vcc
	v_addc_co_u32_e64 v12, s[4:5], 0, v12, s[4:5]
	v_cmp_eq_u32_e64 s[4:5], 4, v61
	s_nop 1
	v_addc_co_u32_e64 v9, s[6:7], 0, v9, s[4:5]
	s_and_b64 s[4:5], s[4:5], vcc
	v_addc_co_u32_e64 v10, s[4:5], 0, v10, s[4:5]
	v_cmp_eq_u32_e64 s[4:5], 5, v61
	s_nop 1
	v_addc_co_u32_e64 v7, s[6:7], 0, v7, s[4:5]
	s_and_b64 s[4:5], s[4:5], vcc
	v_addc_co_u32_e64 v8, s[4:5], 0, v8, s[4:5]
	v_cmp_eq_u32_e64 s[4:5], 6, v61
	s_nop 1
	v_addc_co_u32_e64 v5, s[6:7], 0, v5, s[4:5]
	s_and_b64 s[4:5], s[4:5], vcc
	v_addc_co_u32_e64 v6, s[4:5], 0, v6, s[4:5]
	v_cmp_eq_u32_e64 s[4:5], 7, v61
	s_and_b64 vcc, s[4:5], vcc
	v_addc_co_u32_e32 v4, vcc, 0, v4, vcc
	v_addc_co_u32_e64 v3, s[6:7], 0, v3, s[4:5]
	v_add_u32_e32 v20, 0x200, v20
	v_cmp_gt_i32_e32 vcc, s17, v20
	s_waitcnt vmcnt(1)
	v_cmp_eq_u32_e64 s[4:5], 0, v62
	s_nop 1
	v_addc_co_u32_e64 v18, s[6:7], 0, v18, s[4:5]
	s_and_b64 s[4:5], s[4:5], vcc
	v_addc_co_u32_e64 v19, s[4:5], 0, v19, s[4:5]
	v_cmp_eq_u32_e64 s[4:5], 1, v62
	s_nop 1
	v_addc_co_u32_e64 v15, s[6:7], 0, v15, s[4:5]
	s_and_b64 s[4:5], s[4:5], vcc
	v_addc_co_u32_e64 v16, s[4:5], 0, v16, s[4:5]
	v_cmp_eq_u32_e64 s[4:5], 2, v62
	s_nop 1
	v_addc_co_u32_e64 v13, s[6:7], 0, v13, s[4:5]
	s_and_b64 s[4:5], s[4:5], vcc
	v_addc_co_u32_e64 v14, s[4:5], 0, v14, s[4:5]
	v_cmp_eq_u32_e64 s[4:5], 3, v62
	s_nop 1
	v_addc_co_u32_e64 v11, s[6:7], 0, v11, s[4:5]
	s_and_b64 s[4:5], s[4:5], vcc
	v_addc_co_u32_e64 v12, s[4:5], 0, v12, s[4:5]
	v_cmp_eq_u32_e64 s[4:5], 4, v62
	s_nop 1
	v_addc_co_u32_e64 v9, s[6:7], 0, v9, s[4:5]
	s_and_b64 s[4:5], s[4:5], vcc
	v_addc_co_u32_e64 v10, s[4:5], 0, v10, s[4:5]
	v_cmp_eq_u32_e64 s[4:5], 5, v62
	s_nop 1
	v_addc_co_u32_e64 v7, s[6:7], 0, v7, s[4:5]
	s_and_b64 s[4:5], s[4:5], vcc
	v_addc_co_u32_e64 v8, s[4:5], 0, v8, s[4:5]
	v_cmp_eq_u32_e64 s[4:5], 6, v62
	s_nop 1
	v_addc_co_u32_e64 v5, s[6:7], 0, v5, s[4:5]
	s_and_b64 s[4:5], s[4:5], vcc
	v_addc_co_u32_e64 v6, s[4:5], 0, v6, s[4:5]
	v_cmp_eq_u32_e64 s[4:5], 7, v62
	s_and_b64 vcc, s[4:5], vcc
	v_addc_co_u32_e32 v4, vcc, 0, v4, vcc
	v_addc_co_u32_e64 v3, s[6:7], 0, v3, s[4:5]
	v_add_u32_e32 v20, 0x200, v20
	v_cmp_gt_i32_e32 vcc, s17, v20
	s_waitcnt vmcnt(0)
	v_cmp_eq_u32_e64 s[4:5], 0, v63
	s_nop 1
	v_addc_co_u32_e64 v18, s[6:7], 0, v18, s[4:5]
	s_and_b64 s[4:5], s[4:5], vcc
	v_addc_co_u32_e64 v19, s[4:5], 0, v19, s[4:5]
	v_cmp_eq_u32_e64 s[4:5], 1, v63
	s_nop 1
	v_addc_co_u32_e64 v15, s[6:7], 0, v15, s[4:5]
	s_and_b64 s[4:5], s[4:5], vcc
	v_addc_co_u32_e64 v16, s[4:5], 0, v16, s[4:5]
	v_cmp_eq_u32_e64 s[4:5], 2, v63
	s_nop 1
	v_addc_co_u32_e64 v13, s[6:7], 0, v13, s[4:5]
	s_and_b64 s[4:5], s[4:5], vcc
	v_addc_co_u32_e64 v14, s[4:5], 0, v14, s[4:5]
	v_cmp_eq_u32_e64 s[4:5], 3, v63
	s_nop 1
	v_addc_co_u32_e64 v11, s[6:7], 0, v11, s[4:5]
	s_and_b64 s[4:5], s[4:5], vcc
	v_addc_co_u32_e64 v12, s[4:5], 0, v12, s[4:5]
	v_cmp_eq_u32_e64 s[4:5], 4, v63
	s_nop 1
	v_addc_co_u32_e64 v9, s[6:7], 0, v9, s[4:5]
	s_and_b64 s[4:5], s[4:5], vcc
	v_addc_co_u32_e64 v10, s[4:5], 0, v10, s[4:5]
	v_cmp_eq_u32_e64 s[4:5], 5, v63
	s_nop 1
	v_addc_co_u32_e64 v7, s[6:7], 0, v7, s[4:5]
	s_and_b64 s[4:5], s[4:5], vcc
	v_addc_co_u32_e64 v8, s[4:5], 0, v8, s[4:5]
	v_cmp_eq_u32_e64 s[4:5], 6, v63
	s_nop 1
	v_addc_co_u32_e64 v5, s[6:7], 0, v5, s[4:5]
	s_and_b64 s[4:5], s[4:5], vcc
	v_addc_co_u32_e64 v6, s[4:5], 0, v6, s[4:5]
	v_cmp_eq_u32_e64 s[4:5], 7, v63
	s_and_b64 vcc, s[4:5], vcc
	v_addc_co_u32_e32 v4, vcc, 0, v4, vcc
	v_addc_co_u32_e64 v3, s[6:7], 0, v3, s[4:5]
	s_mov_b64 s[14:15], exec
	s_or_b64 exec, exec, s[14:15]
